# PLE bf16 epilogue: next batch's 10 loads issued one batch early (software pipelined), on top of rstd de-serialisation
# speedup vs baseline: 1.0039x; 1.0039x over previous
; template <int MASK> __device__ __forceinline__ float swz_f(float v) { return __builtin_bit_cast(float, __builtin_amdgcn_ds_swizzle(__builtin_bit_cast(int, v), (MASK << 10) | 0x1f)); }
; __device__ __forceinline__ float sum_x32(float v) { const unsigned u = __builtin_bit_cast(unsigned, v); auto rr = __builtin_amdgcn_permlane32_swap(u, u, false, false); return __builtin_bit_cast(float, (unsigned)rr[0]) + __builtin_bit_cast(float, (unsigned)rr[1]); }
; __device__ __forceinline__ float fast_sigmoid(float x) { return __builtin_amdgcn_rcpf(1.f + __builtin_amdgcn_exp2f(-LOG2E * x)); }
; __device__ __forceinline__ float rstd_q(const float* ssq, int row, int fq) {
;     const f32x4 p = *(const f32x4*)(ssq + 16 * (size_t)row + 4 * fq); float s = (p.x + p.y) + (p.z + p.w); s += swz_f<16>(s); s = sum_x32(s);
;     return __builtin_amdgcn_rsqf(s * (1.f / 1024.f) + EPS);
;     __device__ __forceinline__ void operator()(const f32x4 (&acc)[2][2][4][2], const Unit& u, int wr, int wc, int fr, int fq) const {
;     ...
;         for (int mb = 0; mb < 4; mb += MBAT) {
;             u32x4 hv[4][2], pv[4][2]; float rs4[4];
; #pragma unroll
;             for (int m = mb; m < mb + MBAT; ++m) { const int row = EPI_ROWS(ai, m); rs4[m] = 0.f; if (MODE == 1) rs4[m] = rstd_q(ssq_in, row, fq) * ascale;
; #pragma unroll
;                 for (int bj = 0; bj < 2; ++bj) { const size_t off = (size_t)row * DM + u.pn * BM + bj * HALF + wc * 32 + 8 * fq; hv[m][bj] = *(const u32x4*)(hin + off); if (MODE == 1) pv[m][bj] = *(const u32x4*)(PP + off); } }
; #pragma unroll
;             for (int m = mb; m < mb + MBAT; ++m) { const int row = EPI_ROWS(ai, m); const float rs = rs4[m]; float ss = 0.f;
; #pragma unroll
;                 for (int bj = 0; bj < 2; ++bj) { const size_t off = (size_t)row * DM + u.pn * BM + bj * HALF + wc * 32 + 8 * fq;
;                     f32x4 v0, v1; unpack8(hv[m][bj], v0, v1); const f32x4 a0 = acc[ai][bj][m][0], a1 = acc[ai][bj][m][1];
;                     if (MODE == 0) { v0 = v0 + a0 * ascale; v1 = v1 + a1 * ascale; }
;                     else { f32x4 p0, p1; unpack8(pv[m][bj], p0, p1);
; #pragma unroll
;                         for (int e = 0; e < 4; ++e) { v0[e] += fast_sigmoid(a0[e] * rs) * p0[e]; v1[e] += fast_sigmoid(a1[e] * rs) * p1[e]; } }
.LBB0_1947:
	s_lshl_b32 s6, s28, 8
	v_mov_b32_e32 v124, v172
	v_mov_b32_e32 v125, v173
	s_add_i32 s6, s6, s76
	s_waitcnt vmcnt(22)
	v_lshlrev_b32_e32 v120, 2, v125
	v_add_u32_e32 v158, s6, v124
	v_ashrrev_i32_e32 v121, 31, v120
	v_ashrrev_i32_e32 v159, 31, v158
	v_lshlrev_b32_e32 v122, 3, v125
	v_lshl_add_u64 v[156:157], v[120:121], 2, s[16:17]
	v_lshlrev_b64 v[162:163], 6, v[158:159]
	v_ashrrev_i32_e32 v123, 31, v122
	v_lshl_add_u64 v[120:121], v[156:157], 0, v[162:163]
	v_lshl_add_u64 v[152:153], v[122:123], 0, s[20:21]
	global_load_dwordx4 v[120:123], v[120:121], off
	s_lshl_b32 s6, s31, 8
	s_ashr_i32 s7, s6, 31
	v_lshl_add_u64 v[154:155], v[152:153], 0, s[6:7]
	v_lshlrev_b32_e32 v226, 10, v158
	v_lshlrev_b32_e32 v227, 6, v158
	v_add_lshl_u32 v226, v226, v154, 1
	v_lshl_add_u32 v227, v173, 4, v227
	v_lshlrev_b64 v[166:167], 10, v[158:159]
	v_add_u32_e32 v124, 16, v158
	v_cmp_eq_u32_e32 vcc, 0, v125
	v_ashrrev_i32_e32 v125, 31, v124
	v_lshlrev_b64 v[160:161], 6, v[124:125]
	v_lshlrev_b64 v[164:165], 10, v[124:125]
	s_or_b32 s95, s6, 0x80
	s_add_u32 s28, s18, s95
	s_addc_u32 s29, s19, s7
	s_mov_b32 s96, s7
	s_waitcnt vmcnt(0)
	v_add_f32_e32 v120, v120, v121
	v_add_f32_e32 v121, v122, v123
	v_add_f32_e32 v120, v120, v121
	ds_swizzle_b32 v121, v120 offset:swizzle(SWAP,16)
	s_waitcnt lgkmcnt(0)
	v_add_f32_e32 v120, v120, v121
	v_mov_b32_e32 v121, v120
	s_nop 1
	v_permlane32_swap_b32_e32 v120, v121
	v_add_f32_e32 v120, v120, v121
	v_fmamk_f32 v120, v120, 0x3a800000, v230
	v_rsq_f32_e32 v177, v120
	v_lshl_add_u64 v[120:121], v[166:167], 0, v[154:155]
	v_lshlrev_b64 v[120:121], 1, v[120:121]
	v_lshl_add_u64 v[122:123], s[2:3], 0, v[120:121]
	global_load_dwordx4 v[178:181], v[122:123], off
	v_lshl_add_u64 v[120:121], s[14:15], 0, v[120:121]
	global_load_dwordx4 v[182:185], v[120:121], off
	global_load_dwordx4 v[148:151], v[122:123], off offset:256
	global_load_dwordx4 v[144:147], v[120:121], off offset:256
	v_lshl_add_u64 v[120:121], v[156:157], 0, v[160:161]
	global_load_dwordx4 v[120:123], v[120:121], off
	v_mul_f32_e32 v128, v128, v177
	v_mul_f32_e32 v128, 0xbfb8aa3b, v128
	v_exp_f32_e32 v128, v128
	v_mul_f32_e32 v140, v140, v177
	v_mul_f32_e32 v140, 0xbfb8aa3b, v140
	v_exp_f32_e32 v140, v140
	v_add_f32_e32 v128, 1.0, v128
	v_rcp_f32_e32 v128, v128
	v_lshl_add_u64 v[166:167], v[166:167], 0, v[152:153]
	v_add_f32_e32 v140, 1.0, v140
	v_rcp_f32_e32 v140, v140
	v_mul_f32_e32 v112, v112, v177
	v_mul_f32_e32 v112, 0xbfb8aa3b, v112
	v_exp_f32_e32 v112, v112
	v_mul_f32_e32 v116, v116, v177
	v_mul_f32_e32 v116, 0xbfb8aa3b, v116
	v_exp_f32_e32 v116, v116
	v_add_f32_e32 v112, 1.0, v112
	v_rcp_f32_e32 v112, v112
	v_add_f32_e32 v116, 1.0, v116
	v_rcp_f32_e32 v116, v116
	s_waitcnt vmcnt(3)
	v_lshlrev_b32_e32 v192, 16, v184
	v_lshlrev_b32_e32 v188, 16, v180
	v_fmac_f32_e32 v188, v128, v192
	v_mul_f32_e32 v128, v141, v177
	v_mul_f32_e32 v128, 0xbfb8aa3b, v128
	v_exp_f32_e32 v128, v128
	v_lshlrev_b32_e32 v186, 16, v178
	v_and_b32_e32 v178, 0xffff0000, v178
	v_lshlrev_b32_e32 v190, 16, v182
	v_add_f32_e32 v128, 1.0, v128
	v_rcp_f32_e32 v128, v128
	v_and_b32_e32 v182, 0xffff0000, v182
	v_and_b32_e32 v180, 0xffff0000, v180
	v_and_b32_e32 v184, 0xffff0000, v184
	v_fmac_f32_e32 v178, v128, v182
	v_mul_f32_e32 v128, v129, v177
	v_mul_f32_e32 v128, 0xbfb8aa3b, v128
	v_exp_f32_e32 v128, v128
	v_lshlrev_b32_e32 v187, 16, v179
	v_lshlrev_b32_e32 v191, 16, v183
	v_lshlrev_b32_e32 v189, 16, v181
	v_add_f32_e32 v128, 1.0, v128
	v_rcp_f32_e32 v128, v128
	v_lshlrev_b32_e32 v193, 16, v185
	v_and_b32_e32 v179, 0xffff0000, v179
	v_and_b32_e32 v183, 0xffff0000, v183
	v_fmac_f32_e32 v180, v128, v184
	v_mul_f32_e32 v128, v142, v177
	v_mul_f32_e32 v128, 0xbfb8aa3b, v128
	v_exp_f32_e32 v128, v128
	s_waitcnt vmcnt(0)
	v_add_f32_e32 v120, v120, v121
	v_add_f32_e32 v121, v122, v123
	v_add_f32_e32 v120, v120, v121
	v_add_f32_e32 v128, 1.0, v128
	v_rcp_f32_e32 v128, v128
	ds_swizzle_b32 v121, v120 offset:swizzle(SWAP,16)
	v_and_b32_e32 v181, 0xffff0000, v181
	v_and_b32_e32 v185, 0xffff0000, v185
	v_fmac_f32_e32 v187, v128, v191
	v_mul_f32_e32 v128, v130, v177
	v_mul_f32_e32 v128, 0xbfb8aa3b, v128
	v_exp_f32_e32 v128, v128
	s_waitcnt lgkmcnt(0)
	v_add_f32_e32 v159, v120, v121
	v_lshl_add_u64 v[120:121], v[164:165], 0, v[154:155]
	v_lshlrev_b64 v[120:121], 1, v[120:121]
	v_add_f32_e32 v128, 1.0, v128
	v_rcp_f32_e32 v128, v128
	v_lshl_add_u64 v[122:123], s[2:3], 0, v[120:121]
	v_lshl_add_u64 v[120:121], s[14:15], 0, v[120:121]
	global_load_dwordx4 v[136:139], v[122:123], off
	v_fmac_f32_e32 v189, v128, v193
	v_mul_f32_e32 v128, v143, v177
	v_mul_f32_e32 v128, 0xbfb8aa3b, v128
	v_exp_f32_e32 v128, v128
	global_load_dwordx4 v[132:135], v[120:121], off
	global_load_dwordx4 v[124:127], v[122:123], off offset:256
	s_nop 0
	global_load_dwordx4 v[120:123], v[120:121], off offset:256
	v_add_u32_e32 v228, 0x800, v227
	v_add_u32_e32 v229, 0x10000, v226
	global_load_dwordx4 v[200:203], v228, s[16:17]
	global_load_dwordx4 v[204:207], v229, s[2:3]
	global_load_dwordx4 v[208:211], v229, s[14:15]
	global_load_dwordx4 v[212:215], v229, s[2:3] offset:256
	global_load_dwordx4 v[216:219], v229, s[14:15] offset:256
	global_load_dwordx4 v[220:223], v228, s[16:17] offset:1024
	v_add_u32_e32 v225, 0x18000, v226
	global_load_dwordx4 v[236:239], v225, s[2:3]
	global_load_dwordx4 v[240:243], v225, s[14:15]
	global_load_dwordx4 v[244:247], v225, s[2:3] offset:256
	global_load_dwordx4 v[248:251], v225, s[14:15] offset:256
	v_fmac_f32_e32 v186, v140, v190
	v_cvt_pk_bf16_f32 v140, v186, v178
	v_add_f32_e32 v128, 1.0, v128
	v_rcp_f32_e32 v128, v128
	v_mov_b32_e32 v176, v159
	s_nop 1
	v_permlane32_swap_b32_e32 v159, v176
; template <int MASK> __device__ __forceinline__ float swz_f(float v) { return __builtin_bit_cast(float, __builtin_amdgcn_ds_swizzle(__builtin_bit_cast(int, v), (MASK << 10) | 0x1f)); }
; __device__ __forceinline__ float sum_x32(float v) { const unsigned u = __builtin_bit_cast(unsigned, v); auto rr = __builtin_amdgcn_permlane32_swap(u, u, false, false); return __builtin_bit_cast(float, (unsigned)rr[0]) + __builtin_bit_cast(float, (unsigned)rr[1]); }
; __device__ __forceinline__ float fast_sigmoid(float x) { return __builtin_amdgcn_rcpf(1.f + __builtin_amdgcn_exp2f(-LOG2E * x)); }
; __device__ __forceinline__ u32x4 pack8(const f32x4 a, const f32x4 b) { u32x4 w; w.x = cvt_pk_bf16(a[0], a[1]); w.y = cvt_pk_bf16(a[2], a[3]); w.z = cvt_pk_bf16(b[0], b[1]); w.w = cvt_pk_bf16(b[2], b[3]); return w; }
;     __device__ __forceinline__ void operator()(const f32x4 (&acc)[2][2][4][2], const Unit& u, int wr, int wc, int fr, int fq) const {
;     ...
;             for (int m = mb; m < mb + MBAT; ++m) { const int row = EPI_ROWS(ai, m); const float rs = rs4[m]; float ss = 0.f;
; #pragma unroll
;                 for (int bj = 0; bj < 2; ++bj) { const size_t off = (size_t)row * DM + u.pn * BM + bj * HALF + wc * 32 + 8 * fq;
;                     f32x4 v0, v1; unpack8(hv[m][bj], v0, v1); const f32x4 a0 = acc[ai][bj][m][0], a1 = acc[ai][bj][m][1];
;                     if (MODE == 0) { v0 = v0 + a0 * ascale; v1 = v1 + a1 * ascale; }
;                     else { f32x4 p0, p1; unpack8(pv[m][bj], p0, p1);
; #pragma unroll
;                         for (int e = 0; e < 4; ++e) { v0[e] += fast_sigmoid(a0[e] * rs) * p0[e]; v1[e] += fast_sigmoid(a1[e] * rs) * p1[e]; } }
;                     if (outf) { *(f32x4*)(outf + off) = v0; *(f32x4*)(outf + off + 4) = v1; }
;                     else *(u32x4*)(hout + off) = pack8(v0, v1);
;                     if (h8) { u32x2 w8; w8.x = pk4_fp8(v0[0], v0[1], v0[2], v0[3]); w8.y = pk4_fp8(v1[0], v1[1], v1[2], v1[3]); *(u32x2*)(h8 + off) = w8; }
;                     ss += ((v0[0] * v0[0] + v0[1] * v0[1]) + (v0[2] * v0[2] + v0[3] * v0[3])) + ((v1[0] * v1[0] + v1[1] * v1[1]) + (v1[2] * v1[2] + v1[3] * v1[3])); }
;                 ss += swz_f<16>(ss); ss = sum_x32(ss);
;                 if (fq == 0) ssq_out[(size_t)row * 16 + u.pn * 4 + wc] = ss; }
	v_fmac_f32_e32 v179, v128, v183
	v_mul_f32_e32 v128, v131, v177
	v_mul_f32_e32 v128, 0xbfb8aa3b, v128
	v_exp_f32_e32 v128, v128
	v_lshl_add_u64 v[130:131], v[166:167], 0, s[6:7]
	v_cvt_pk_bf16_f32 v141, v187, v179
	v_cvt_pk_bf16_f32 v142, v188, v180
	v_add_f32_e32 v128, 1.0, v128
	v_rcp_f32_e32 v128, v128
	s_nop 0
	v_fmac_f32_e32 v181, v128, v185
	v_lshl_add_u64 v[128:129], v[130:131], 1, s[10:11]
	v_cvt_pk_bf16_f32 v143, v189, v181
	global_store_dwordx4 v[128:129], v[140:143], off
	v_med3_f32 v182, v181, s49, v254
	v_lshl_add_u64 v[130:131], s[18:19], 0, v[130:131]
	v_med3_f32 v140, v186, s49, v254
	v_med3_f32 v141, v178, s49, v254
	v_cvt_pk_fp8_f32 v140, v140, v141
	v_med3_f32 v142, v187, s49, v254
	v_med3_f32 v143, v179, s49, v254
	v_med3_f32 v141, v188, s49, v254
	v_cvt_pk_fp8_f32 v140, v142, v143 op_sel:[0,0,1]
	v_med3_f32 v142, v180, s49, v254
	v_cvt_pk_fp8_f32 v141, v141, v142
	v_med3_f32 v143, v189, s49, v254
	v_and_b32_e32 v142, 0xffff0000, v149
	v_cvt_pk_fp8_f32 v141, v143, v182 op_sel:[0,0,1]
	v_lshlrev_b32_e32 v143, 16, v150
	global_store_dwordx2 v[130:131], v[140:141], off
	v_mul_f32_e32 v131, v179, v179
	v_lshlrev_b32_e32 v179, 16, v146
	v_fmac_f32_e32 v143, v112, v179
	v_mul_f32_e32 v112, v117, v177
	v_mul_f32_e32 v112, 0xbfb8aa3b, v112
	v_exp_f32_e32 v112, v112
	v_mul_f32_e32 v130, v178, v178
	v_fmac_f32_e32 v130, v186, v186
	v_fmac_f32_e32 v131, v187, v187
	v_add_f32_e32 v112, 1.0, v112
	v_add_f32_e32 v130, v130, v131
	v_mul_f32_e32 v131, v180, v180
	v_mul_f32_e32 v140, v181, v181
	v_rcp_f32_e32 v112, v112
	v_fmac_f32_e32 v131, v188, v188
	v_fmac_f32_e32 v140, v189, v189
	v_add_f32_e32 v131, v131, v140
	v_add_f32_e32 v130, v130, v131
	v_lshlrev_b32_e32 v131, 16, v148
	v_and_b32_e32 v140, 0xffff0000, v148
	v_lshlrev_b32_e32 v141, 16, v149
	v_and_b32_e32 v148, 0xffff0000, v150
	v_lshlrev_b32_e32 v149, 16, v151
	v_and_b32_e32 v150, 0xffff0000, v151
	v_lshlrev_b32_e32 v151, 16, v144
	v_and_b32_e32 v144, 0xffff0000, v144
	v_fmac_f32_e32 v140, v112, v144
	v_mul_f32_e32 v112, v113, v177
	v_mul_f32_e32 v112, 0xbfb8aa3b, v112
	v_exp_f32_e32 v112, v112
	v_and_b32_e32 v146, 0xffff0000, v146
	v_lshlrev_b32_e32 v178, 16, v145
	v_lshlrev_b32_e32 v180, 16, v147
	v_add_f32_e32 v112, 1.0, v112
	v_rcp_f32_e32 v112, v112
	v_and_b32_e32 v145, 0xffff0000, v145
	v_and_b32_e32 v147, 0xffff0000, v147
	v_fmac_f32_e32 v131, v116, v151
	v_fmac_f32_e32 v148, v112, v146
	v_mul_f32_e32 v112, v118, v177
	v_mul_f32_e32 v112, 0xbfb8aa3b, v112
	v_exp_f32_e32 v112, v112
	s_nop 0
	v_add_f32_e32 v112, 1.0, v112
	v_rcp_f32_e32 v112, v112
	s_nop 0
	v_fmac_f32_e32 v141, v112, v178
	v_mul_f32_e32 v112, v114, v177
	v_mul_f32_e32 v112, 0xbfb8aa3b, v112
	v_exp_f32_e32 v112, v112
	s_nop 0
	v_add_f32_e32 v112, 1.0, v112
	v_rcp_f32_e32 v112, v112
	s_nop 0
	v_fmac_f32_e32 v149, v112, v180
	v_mul_f32_e32 v112, v119, v177
	v_mul_f32_e32 v112, 0xbfb8aa3b, v112
	v_exp_f32_e32 v112, v112
	s_nop 0
	v_add_f32_e32 v112, 1.0, v112
	v_rcp_f32_e32 v112, v112
	s_nop 0
	v_fmac_f32_e32 v142, v112, v145
	v_mul_f32_e32 v112, v115, v177
	v_mul_f32_e32 v112, 0xbfb8aa3b, v112
	v_exp_f32_e32 v112, v112
	s_nop 0
	v_add_f32_e32 v112, 1.0, v112
	v_rcp_f32_e32 v112, v112
	s_nop 0
	v_fmac_f32_e32 v150, v112, v147
	v_cvt_pk_bf16_f32 v112, v131, v140
	v_cvt_pk_bf16_f32 v113, v141, v142
	v_cvt_pk_bf16_f32 v114, v143, v148
	v_cvt_pk_bf16_f32 v115, v149, v150
	global_store_dwordx4 v[128:129], v[112:115], off offset:256
	v_med3_f32 v116, v150, s49, v254
	s_nop 0
	v_med3_f32 v112, v131, s49, v254
	v_med3_f32 v113, v140, s49, v254
	v_cvt_pk_fp8_f32 v112, v112, v113
	v_med3_f32 v114, v141, s49, v254
	v_med3_f32 v115, v142, s49, v254
	v_med3_f32 v113, v143, s49, v254
	v_cvt_pk_fp8_f32 v112, v114, v115 op_sel:[0,0,1]
	v_med3_f32 v114, v148, s49, v254
	v_cvt_pk_fp8_f32 v113, v113, v114
	v_med3_f32 v115, v149, s49, v254
	v_cvt_pk_fp8_f32 v113, v115, v116 op_sel:[0,0,1]
	v_lshl_add_u64 v[114:115], s[28:29], 0, v[166:167]
	global_store_dwordx2 v[114:115], v[112:113], off
	v_mul_f32_e32 v112, v140, v140
	v_mul_f32_e32 v113, v142, v142
	v_fmac_f32_e32 v112, v131, v131
	v_fmac_f32_e32 v113, v141, v141
	v_add_f32_e32 v112, v112, v113
	v_mul_f32_e32 v113, v148, v148
	v_mul_f32_e32 v114, v150, v150
	v_fmac_f32_e32 v113, v143, v143
	v_fmac_f32_e32 v114, v149, v149
	v_add_f32_e32 v113, v113, v114
	v_add_f32_e32 v112, v112, v113
	v_add_f32_e32 v112, v130, v112
	ds_swizzle_b32 v113, v112 offset:swizzle(SWAP,16)
	s_waitcnt lgkmcnt(0)
	v_add_f32_e32 v112, v112, v113
	v_mov_b32_e32 v113, v112
	s_nop 1
	v_permlane32_swap_b32_e32 v112, v113
	s_and_saveexec_b64 s[28:29], vcc
	s_cbranch_execz .LBB0_1949
	s_lshl_b32 s54, s31, 2
	v_add_f32_e32 v114, v112, v113
	s_ashr_i32 s55, s54, 31
	v_lshl_add_u64 v[112:113], s[12:13], 0, v[162:163]
	v_lshl_add_u64 v[112:113], s[54:55], 2, v[112:113]
	s_lshl_b32 s54, s59, 2
	s_mov_b32 s55, s40
	v_lshl_add_u64 v[112:113], v[112:113], 0, s[54:55]
	global_store_dword v[112:113], v114, off
; template <int MASK> __device__ __forceinline__ float swz_f(float v) { return __builtin_bit_cast(float, __builtin_amdgcn_ds_swizzle(__builtin_bit_cast(int, v), (MASK << 10) | 0x1f)); }
; __device__ __forceinline__ float sum_x32(float v) { const unsigned u = __builtin_bit_cast(unsigned, v); auto rr = __builtin_amdgcn_permlane32_swap(u, u, false, false); return __builtin_bit_cast(float, (unsigned)rr[0]) + __builtin_bit_cast(float, (unsigned)rr[1]); }
; __device__ __forceinline__ float fast_sigmoid(float x) { return __builtin_amdgcn_rcpf(1.f + __builtin_amdgcn_exp2f(-LOG2E * x)); }
; __device__ __forceinline__ u32x4 pack8(const f32x4 a, const f32x4 b) { u32x4 w; w.x = cvt_pk_bf16(a[0], a[1]); w.y = cvt_pk_bf16(a[2], a[3]); w.z = cvt_pk_bf16(b[0], b[1]); w.w = cvt_pk_bf16(b[2], b[3]); return w; }
;     __device__ __forceinline__ void operator()(const f32x4 (&acc)[2][2][4][2], const Unit& u, int wr, int wc, int fr, int fq) const {
;     ...
;             for (int m = mb; m < mb + MBAT; ++m) { const int row = EPI_ROWS(ai, m); const float rs = rs4[m]; float ss = 0.f;
; #pragma unroll
;                 for (int bj = 0; bj < 2; ++bj) { const size_t off = (size_t)row * DM + u.pn * BM + bj * HALF + wc * 32 + 8 * fq;
;                     f32x4 v0, v1; unpack8(hv[m][bj], v0, v1); const f32x4 a0 = acc[ai][bj][m][0], a1 = acc[ai][bj][m][1];
;                     if (MODE == 0) { v0 = v0 + a0 * ascale; v1 = v1 + a1 * ascale; }
;                     else { f32x4 p0, p1; unpack8(pv[m][bj], p0, p1);
; #pragma unroll
;                         for (int e = 0; e < 4; ++e) { v0[e] += fast_sigmoid(a0[e] * rs) * p0[e]; v1[e] += fast_sigmoid(a1[e] * rs) * p1[e]; } }
;                     if (outf) { *(f32x4*)(outf + off) = v0; *(f32x4*)(outf + off + 4) = v1; }
;                     else *(u32x4*)(hout + off) = pack8(v0, v1);
;                     if (h8) { u32x2 w8; w8.x = pk4_fp8(v0[0], v0[1], v0[2], v0[3]); w8.y = pk4_fp8(v1[0], v1[1], v1[2], v1[3]); *(u32x2*)(h8 + off) = w8; }
;                     ss += ((v0[0] * v0[0] + v0[1] * v0[1]) + (v0[2] * v0[2] + v0[3] * v0[3])) + ((v1[0] * v1[0] + v1[1] * v1[1]) + (v1[2] * v1[2] + v1[3] * v1[3])); }
;                 ss += swz_f<16>(ss); ss = sum_x32(ss);
;                 if (fq == 0) ssq_out[(size_t)row * 16 + u.pn * 4 + wc] = ss; }
.LBB0_1949:
	s_or_b64 exec, exec, s[28:29]
	v_add_f32_e32 v112, v159, v176
	v_fmamk_f32 v112, v112, 0x3a800000, v230
	v_rsq_f32_e32 v116, v112
	s_waitcnt vmcnt(17)
	v_lshlrev_b32_e32 v119, 16, v137
	v_and_b32_e32 v128, 0xffff0000, v137
	v_lshlrev_b32_e32 v129, 16, v138
	v_mul_f32_e32 v104, v104, v116
	v_mul_f32_e32 v104, 0xbfb8aa3b, v104
	v_exp_f32_e32 v104, v104
	v_mul_f32_e32 v105, v105, v116
	v_mul_f32_e32 v105, 0xbfb8aa3b, v105
	v_exp_f32_e32 v105, v105
	v_add_f32_e32 v104, 1.0, v104
	v_rcp_f32_e32 v104, v104
	s_waitcnt vmcnt(16)
	v_lshlrev_b32_e32 v137, 16, v134
	v_mul_f32_e32 v106, v106, v116
	v_mul_f32_e32 v106, 0xbfb8aa3b, v106
	v_fmac_f32_e32 v129, v104, v137
	v_add_f32_e32 v104, 1.0, v105
	v_mul_f32_e32 v105, v110, v116
	v_mul_f32_e32 v105, 0xbfb8aa3b, v105
	v_mul_f32_e32 v108, v108, v116
	v_mul_f32_e32 v109, v109, v116
	v_rcp_f32_e32 v104, v104
	v_exp_f32_e32 v105, v105
	v_exp_f32_e32 v106, v106
	v_mul_f32_e32 v108, 0xbfb8aa3b, v108
	v_mul_f32_e32 v109, 0xbfb8aa3b, v109
	v_exp_f32_e32 v108, v108
	v_exp_f32_e32 v109, v109
	v_and_b32_e32 v130, 0xffff0000, v138
	v_and_b32_e32 v134, 0xffff0000, v134
	v_fmac_f32_e32 v130, v104, v134
	v_add_f32_e32 v104, 1.0, v105
	v_add_f32_e32 v105, 1.0, v106
	v_mul_f32_e32 v106, v111, v116
	v_mul_f32_e32 v106, 0xbfb8aa3b, v106
	v_mul_f32_e32 v107, v107, v116
	v_add_f32_e32 v108, 1.0, v108
	v_add_f32_e32 v109, 1.0, v109
	v_exp_f32_e32 v106, v106
	v_mul_f32_e32 v107, 0xbfb8aa3b, v107
	v_rcp_f32_e32 v108, v108
	v_rcp_f32_e32 v109, v109
	v_exp_f32_e32 v107, v107
	v_rcp_f32_e32 v104, v104
	v_lshlrev_b32_e32 v117, 16, v136
	v_and_b32_e32 v118, 0xffff0000, v136
	v_lshlrev_b32_e32 v114, 16, v132
	v_and_b32_e32 v115, 0xffff0000, v132
	v_add_f32_e32 v106, 1.0, v106
	v_fmac_f32_e32 v117, v108, v114
	v_fmac_f32_e32 v118, v109, v115
	v_rcp_f32_e32 v106, v106
	v_add_f32_e32 v107, 1.0, v107
	v_lshlrev_b32_e32 v132, 16, v133
	v_rcp_f32_e32 v105, v105
	v_rcp_f32_e32 v107, v107
	v_med3_f32 v110, v117, s49, v254
	v_med3_f32 v111, v118, s49, v254
	v_fmac_f32_e32 v119, v104, v132
	v_cvt_pk_fp8_f32 v110, v110, v111
	v_med3_f32 v111, v129, s49, v254
	v_med3_f32 v132, v130, s49, v254
	v_and_b32_e32 v133, 0xffff0000, v133
	v_cvt_pk_fp8_f32 v111, v111, v132
	v_lshlrev_b32_e32 v131, 16, v139
	v_and_b32_e32 v136, 0xffff0000, v139
	v_lshlrev_b32_e32 v138, 16, v135
	v_and_b32_e32 v135, 0xffff0000, v135
	v_fmac_f32_e32 v128, v106, v133
	v_fmac_f32_e32 v131, v105, v138
	v_fmac_f32_e32 v136, v107, v135
	v_med3_f32 v114, v119, s49, v254
	v_med3_f32 v115, v128, s49, v254
	v_cvt_pk_fp8_f32 v110, v114, v115 op_sel:[0,0,1]
	v_med3_f32 v114, v131, s49, v254
	v_med3_f32 v115, v136, s49, v254
	v_mul_f32_e32 v96, v96, v116
	v_lshl_add_u64 v[112:113], v[164:165], 0, v[152:153]
	v_cvt_pk_fp8_f32 v111, v114, v115 op_sel:[0,0,1]
	v_mul_f32_e32 v96, 0xbfb8aa3b, v96
	v_lshl_add_u64 v[108:109], v[112:113], 0, s[6:7]
	v_exp_f32_e32 v96, v96
	v_cvt_pk_bf16_f32 v104, v117, v118
	v_cvt_pk_bf16_f32 v105, v119, v128
	v_lshl_add_u64 v[114:115], v[108:109], 1, s[10:11]
	v_cvt_pk_bf16_f32 v106, v129, v130
	v_cvt_pk_bf16_f32 v107, v131, v136
	global_store_dwordx4 v[114:115], v[104:107], off
	v_mul_f32_e32 v97, v97, v116
	v_add_f32_e32 v96, 1.0, v96
	v_lshl_add_u64 v[104:105], s[18:19], 0, v[108:109]
	global_store_dwordx2 v[104:105], v[110:111], off
	v_mul_f32_e32 v104, v118, v118
	v_mul_f32_e32 v105, v128, v128
	v_fmac_f32_e32 v104, v117, v117
	v_fmac_f32_e32 v105, v119, v119
	v_mul_f32_e32 v97, 0xbfb8aa3b, v97
	v_add_f32_e32 v104, v104, v105
	v_mul_f32_e32 v105, v130, v130
	v_mul_f32_e32 v106, v136, v136
	v_rcp_f32_e32 v96, v96
	v_exp_f32_e32 v97, v97
	v_fmac_f32_e32 v105, v129, v129
	v_fmac_f32_e32 v106, v131, v131
	v_add_f32_e32 v105, v105, v106
	v_add_f32_e32 v104, v104, v105
	s_waitcnt vmcnt(17)
	v_lshlrev_b32_e32 v105, 16, v124
	v_and_b32_e32 v106, 0xffff0000, v124
	v_lshlrev_b32_e32 v109, 16, v126
	s_waitcnt vmcnt(16)
	v_lshlrev_b32_e32 v124, 16, v122
	v_fmac_f32_e32 v109, v96, v124
	v_add_f32_e32 v96, 1.0, v97
	v_mul_f32_e32 v97, v102, v116
	v_mul_f32_e32 v98, v98, v116
	v_mul_f32_e32 v97, 0xbfb8aa3b, v97
	v_mul_f32_e32 v98, 0xbfb8aa3b, v98
	v_rcp_f32_e32 v96, v96
	v_exp_f32_e32 v97, v97
	v_exp_f32_e32 v98, v98
	v_and_b32_e32 v110, 0xffff0000, v126
	v_and_b32_e32 v122, 0xffff0000, v122
	v_mul_f32_e32 v100, v100, v116
	v_mul_f32_e32 v101, v101, v116
	v_fmac_f32_e32 v110, v96, v122
	v_add_f32_e32 v96, 1.0, v97
	v_add_f32_e32 v97, 1.0, v98
	v_mul_f32_e32 v98, v103, v116
	v_mul_f32_e32 v100, 0xbfb8aa3b, v100
	v_mul_f32_e32 v101, 0xbfb8aa3b, v101
	v_mul_f32_e32 v98, 0xbfb8aa3b, v98
	v_mul_f32_e32 v99, v99, v116
	v_exp_f32_e32 v100, v100
	v_exp_f32_e32 v101, v101
	v_exp_f32_e32 v98, v98
	v_mul_f32_e32 v99, 0xbfb8aa3b, v99
	v_exp_f32_e32 v99, v99
	v_add_f32_e32 v100, 1.0, v100
	v_add_f32_e32 v101, 1.0, v101
	v_add_f32_e32 v98, 1.0, v98
	v_rcp_f32_e32 v100, v100
	v_rcp_f32_e32 v101, v101
	v_rcp_f32_e32 v96, v96
	v_rcp_f32_e32 v97, v97
	v_rcp_f32_e32 v98, v98
	v_add_f32_e32 v99, 1.0, v99
	v_rcp_f32_e32 v99, v99
	v_lshlrev_b32_e32 v107, 16, v125
	v_and_b32_e32 v108, 0xffff0000, v125
	v_lshlrev_b32_e32 v111, 16, v127
	v_lshlrev_b32_e32 v118, 16, v120
	v_and_b32_e32 v119, 0xffff0000, v120
	v_lshlrev_b32_e32 v120, 16, v121
	v_and_b32_e32 v121, 0xffff0000, v121
	v_lshlrev_b32_e32 v125, 16, v123
	v_and_b32_e32 v117, 0xffff0000, v127
	v_and_b32_e32 v123, 0xffff0000, v123
	v_fmac_f32_e32 v105, v100, v118
	v_fmac_f32_e32 v106, v101, v119
	v_fmac_f32_e32 v107, v96, v120
	v_fmac_f32_e32 v111, v97, v125
	v_fmac_f32_e32 v108, v98, v121
	v_cvt_pk_bf16_f32 v96, v105, v106
	v_cvt_pk_bf16_f32 v97, v107, v108
	v_fmac_f32_e32 v117, v99, v123
	v_cvt_pk_bf16_f32 v98, v109, v110
	v_cvt_pk_bf16_f32 v99, v111, v117
	global_store_dwordx4 v[114:115], v[96:99], off offset:256
	v_med3_f32 v100, v110, s49, v254
	s_add_u32 s28, s18, s95
	v_med3_f32 v96, v105, s49, v254
	v_med3_f32 v97, v106, s49, v254
	v_cvt_pk_fp8_f32 v96, v96, v97
	v_med3_f32 v97, v109, s49, v254
	v_cvt_pk_fp8_f32 v97, v97, v100
	v_med3_f32 v98, v107, s49, v254
	v_med3_f32 v99, v108, s49, v254
	v_cvt_pk_fp8_f32 v96, v98, v99 op_sel:[0,0,1]
	v_med3_f32 v98, v111, s49, v254
	v_med3_f32 v99, v117, s49, v254
	v_cvt_pk_fp8_f32 v97, v98, v99 op_sel:[0,0,1]
	v_mul_f32_e32 v98, v106, v106
	v_mul_f32_e32 v99, v108, v108
	v_fmac_f32_e32 v98, v105, v105
	v_fmac_f32_e32 v99, v107, v107
	v_add_f32_e32 v98, v98, v99
	v_mul_f32_e32 v99, v110, v110
	v_mul_f32_e32 v100, v117, v117
	v_fmac_f32_e32 v99, v109, v109
	v_fmac_f32_e32 v100, v111, v111
	v_add_f32_e32 v99, v99, v100
	v_add_f32_e32 v98, v98, v99
	v_add_f32_e32 v100, v104, v98
	ds_swizzle_b32 v101, v100 offset:swizzle(SWAP,16)
	s_addc_u32 s29, s19, s96
	v_lshl_add_u64 v[98:99], s[28:29], 0, v[112:113]
	global_store_dwordx2 v[98:99], v[96:97], off
	s_waitcnt lgkmcnt(0)
	v_add_f32_e32 v96, v100, v101
	v_mov_b32_e32 v97, v96
	s_nop 1
	v_permlane32_swap_b32_e32 v96, v97
	s_and_saveexec_b64 s[28:29], vcc
	s_cbranch_execz .LBB0_1951
; __device__ __forceinline__ float fast_sigmoid(float x) { return __builtin_amdgcn_rcpf(1.f + __builtin_amdgcn_exp2f(-LOG2E * x)); }
;     __device__ __forceinline__ void operator()(const f32x4 (&acc)[2][2][4][2], const Unit& u, int wr, int wc, int fr, int fq) const {
;     ...
;         for (int mb = 0; mb < 4; mb += MBAT) {
;             u32x4 hv[4][2], pv[4][2]; float rs4[4];
; #pragma unroll
;             for (int m = mb; m < mb + MBAT; ++m) { const int row = EPI_ROWS(ai, m); rs4[m] = 0.f; if (MODE == 1) rs4[m] = rstd_q(ssq_in, row, fq) * ascale;
; #pragma unroll
;                 for (int bj = 0; bj < 2; ++bj) { const size_t off = (size_t)row * DM + u.pn * BM + bj * HALF + wc * 32 + 8 * fq; hv[m][bj] = *(const u32x4*)(hin + off); if (MODE == 1) pv[m][bj] = *(const u32x4*)(PP + off); } }
; #pragma unroll
;             for (int m = mb; m < mb + MBAT; ++m) { const int row = EPI_ROWS(ai, m); const float rs = rs4[m]; float ss = 0.f;
; #pragma unroll
;                 for (int bj = 0; bj < 2; ++bj) { const size_t off = (size_t)row * DM + u.pn * BM + bj * HALF + wc * 32 + 8 * fq;
;                     f32x4 v0, v1; unpack8(hv[m][bj], v0, v1); const f32x4 a0 = acc[ai][bj][m][0], a1 = acc[ai][bj][m][1];
;                     if (MODE == 0) { v0 = v0 + a0 * ascale; v1 = v1 + a1 * ascale; }
;                     else { f32x4 p0, p1; unpack8(pv[m][bj], p0, p1);
; #pragma unroll
;                         for (int e = 0; e < 4; ++e) { v0[e] += fast_sigmoid(a0[e] * rs) * p0[e]; v1[e] += fast_sigmoid(a1[e] * rs) * p1[e]; } }
	s_lshl_b32 s54, s31, 2
	v_add_f32_e32 v98, v96, v97
	s_ashr_i32 s55, s54, 31
	v_lshl_add_u64 v[96:97], s[12:13], 0, v[160:161]
	v_lshl_add_u64 v[96:97], s[54:55], 2, v[96:97]
	s_lshl_b32 s54, s59, 2
	s_mov_b32 s55, s40
	v_lshl_add_u64 v[96:97], v[96:97], 0, s[54:55]
	global_store_dword v[96:97], v98, off
.LBB0_1951:
	s_or_b64 exec, exec, s[28:29]
	v_add_u32_e32 v100, 32, v158
	v_ashrrev_i32_e32 v101, 31, v100
	v_lshlrev_b64 v[122:123], 6, v[100:101]
	v_lshl_add_u64 v[96:97], v[156:157], 0, v[122:123]
	s_nop 0
	v_lshlrev_b64 v[126:127], 10, v[100:101]
	v_add_u32_e32 v100, 48, v158
	v_ashrrev_i32_e32 v101, 31, v100
	v_lshlrev_b64 v[120:121], 6, v[100:101]
	v_lshlrev_b64 v[124:125], 10, v[100:101]
	s_add_u32 s28, s18, s95
	s_addc_u32 s29, s19, s96
	s_waitcnt vmcnt(8)
	v_mov_b32_e32 v96, v200
	v_mov_b32_e32 v97, v201
	v_mov_b32_e32 v98, v202
	v_mov_b32_e32 v99, v203
	v_add_f32_e32 v96, v96, v97
	v_add_f32_e32 v97, v98, v99
	v_add_f32_e32 v96, v96, v97
	ds_swizzle_b32 v97, v96 offset:swizzle(SWAP,16)
	s_waitcnt lgkmcnt(0)
	v_add_f32_e32 v96, v96, v97
	v_mov_b32_e32 v97, v96
	s_nop 1
	v_permlane32_swap_b32_e32 v96, v97
	v_add_f32_e32 v96, v96, v97
	v_fmamk_f32 v96, v96, 0x3a800000, v230
	v_rsq_f32_e32 v130, v96
	v_lshl_add_u64 v[96:97], v[126:127], 0, v[154:155]
	v_lshlrev_b64 v[96:97], 1, v[96:97]
	v_lshl_add_u64 v[98:99], s[2:3], 0, v[96:97]
	v_mov_b32_e32 v132, v204
	v_mov_b32_e32 v133, v205
	v_mov_b32_e32 v134, v206
	v_mov_b32_e32 v135, v207
	v_lshl_add_u64 v[96:97], s[14:15], 0, v[96:97]
	v_mov_b32_e32 v136, v208
	v_mov_b32_e32 v137, v209
	v_mov_b32_e32 v138, v210
	v_mov_b32_e32 v139, v211
	v_mov_b32_e32 v116, v212
	v_mov_b32_e32 v117, v213
	v_mov_b32_e32 v118, v214
	v_mov_b32_e32 v119, v215
	v_mov_b32_e32 v112, v216
	v_mov_b32_e32 v113, v217
	v_mov_b32_e32 v114, v218
	v_mov_b32_e32 v115, v219
	v_lshl_add_u64 v[96:97], v[156:157], 0, v[120:121]
	v_mov_b32_e32 v96, v220
	v_mov_b32_e32 v97, v221
	v_mov_b32_e32 v98, v222
	v_mov_b32_e32 v99, v223
	v_mul_f32_e32 v88, v88, v130
	v_mul_f32_e32 v88, 0xbfb8aa3b, v88
	v_exp_f32_e32 v88, v88
	v_mul_f32_e32 v92, v92, v130
	v_mul_f32_e32 v92, 0xbfb8aa3b, v92
	v_exp_f32_e32 v92, v92
	v_add_f32_e32 v88, 1.0, v88
	v_rcp_f32_e32 v88, v88
	v_lshl_add_u64 v[126:127], v[126:127], 0, v[152:153]
	v_add_f32_e32 v92, 1.0, v92
	v_rcp_f32_e32 v92, v92
	v_mul_f32_e32 v80, v80, v130
	v_mul_f32_e32 v80, 0xbfb8aa3b, v80
	v_exp_f32_e32 v80, v80
	v_mul_f32_e32 v84, v84, v130
	v_mul_f32_e32 v84, 0xbfb8aa3b, v84
	v_exp_f32_e32 v84, v84
	v_add_f32_e32 v80, 1.0, v80
	v_rcp_f32_e32 v80, v80
	v_add_f32_e32 v84, 1.0, v84
	v_rcp_f32_e32 v84, v84
	s_nop 0
	v_lshlrev_b32_e32 v145, 16, v138
	v_lshlrev_b32_e32 v141, 16, v134
	v_fmac_f32_e32 v141, v88, v145
	v_mul_f32_e32 v88, v93, v130
	v_mul_f32_e32 v88, 0xbfb8aa3b, v88
	v_exp_f32_e32 v88, v88
	v_lshlrev_b32_e32 v131, 16, v132
	v_and_b32_e32 v132, 0xffff0000, v132
	v_lshlrev_b32_e32 v143, 16, v136
	v_add_f32_e32 v88, 1.0, v88
	v_rcp_f32_e32 v88, v88
	v_and_b32_e32 v136, 0xffff0000, v136
	v_and_b32_e32 v134, 0xffff0000, v134
	v_and_b32_e32 v138, 0xffff0000, v138
	v_fmac_f32_e32 v132, v88, v136
	v_mul_f32_e32 v88, v89, v130
	v_mul_f32_e32 v88, 0xbfb8aa3b, v88
	v_exp_f32_e32 v88, v88
	v_lshlrev_b32_e32 v140, 16, v133
	v_lshlrev_b32_e32 v144, 16, v137
	v_lshlrev_b32_e32 v142, 16, v135
	v_add_f32_e32 v88, 1.0, v88
	v_rcp_f32_e32 v88, v88
	v_lshlrev_b32_e32 v146, 16, v139
	v_and_b32_e32 v133, 0xffff0000, v133
	v_and_b32_e32 v137, 0xffff0000, v137
	v_fmac_f32_e32 v134, v88, v138
	v_mul_f32_e32 v88, v94, v130
	v_mul_f32_e32 v88, 0xbfb8aa3b, v88
	v_exp_f32_e32 v88, v88
	s_nop 0
	v_add_f32_e32 v96, v96, v97
	v_add_f32_e32 v97, v98, v99
	v_add_f32_e32 v96, v96, v97
	v_add_f32_e32 v88, 1.0, v88
	v_rcp_f32_e32 v88, v88
	ds_swizzle_b32 v97, v96 offset:swizzle(SWAP,16)
	v_and_b32_e32 v135, 0xffff0000, v135
	v_and_b32_e32 v139, 0xffff0000, v139
	v_fmac_f32_e32 v140, v88, v144
	v_mul_f32_e32 v88, v90, v130
	v_mul_f32_e32 v88, 0xbfb8aa3b, v88
	v_exp_f32_e32 v88, v88
	s_waitcnt lgkmcnt(0)
	v_add_f32_e32 v128, v96, v97
	v_lshl_add_u64 v[96:97], v[124:125], 0, v[154:155]
	v_lshlrev_b64 v[96:97], 1, v[96:97]
	v_add_f32_e32 v88, 1.0, v88
	v_rcp_f32_e32 v88, v88
	v_lshl_add_u64 v[98:99], s[2:3], 0, v[96:97]
	v_lshl_add_u64 v[96:97], s[14:15], 0, v[96:97]
	v_mov_b32_e32 v108, v236
	v_mov_b32_e32 v109, v237
	v_mov_b32_e32 v110, v238
	v_mov_b32_e32 v111, v239
	v_fmac_f32_e32 v142, v88, v146
	v_mul_f32_e32 v88, v95, v130
	v_mul_f32_e32 v88, 0xbfb8aa3b, v88
	v_exp_f32_e32 v88, v88
	v_lshl_add_u64 v[94:95], v[126:127], 0, s[6:7]
	v_mov_b32_e32 v104, v240
	v_mov_b32_e32 v105, v241
	v_mov_b32_e32 v106, v242
	v_mov_b32_e32 v107, v243
	v_mov_b32_e32 v100, v244
	v_mov_b32_e32 v101, v245
	v_mov_b32_e32 v102, v246
	v_mov_b32_e32 v103, v247
	s_nop 0
	v_mov_b32_e32 v96, v248
	v_mov_b32_e32 v97, v249
	v_mov_b32_e32 v98, v250
	v_mov_b32_e32 v99, v251
	v_add_u32_e32 v228, 0x2000, v227
	v_add_u32_e32 v229, 0x40000, v226
	global_load_dwordx4 v[200:203], v228, s[16:17]
	global_load_dwordx4 v[204:207], v229, s[2:3]
	global_load_dwordx4 v[208:211], v229, s[14:15]
	global_load_dwordx4 v[212:215], v229, s[2:3] offset:256
	global_load_dwordx4 v[216:219], v229, s[14:15] offset:256
	global_load_dwordx4 v[220:223], v228, s[16:17] offset:1024
	v_add_u32_e32 v225, 0x48000, v226
	global_load_dwordx4 v[236:239], v225, s[2:3]
	global_load_dwordx4 v[240:243], v225, s[14:15]
	global_load_dwordx4 v[244:247], v225, s[2:3] offset:256
	global_load_dwordx4 v[248:251], v225, s[14:15] offset:256
	v_fmac_f32_e32 v131, v92, v143
	v_add_f32_e32 v88, 1.0, v88
	v_rcp_f32_e32 v88, v88
	v_cvt_pk_bf16_f32 v90, v131, v132
	v_mov_b32_e32 v129, v128
; template <int MASK> __device__ __forceinline__ float swz_f(float v) { return __builtin_bit_cast(float, __builtin_amdgcn_ds_swizzle(__builtin_bit_cast(int, v), (MASK << 10) | 0x1f)); }
; __device__ __forceinline__ float sum_x32(float v) { const unsigned u = __builtin_bit_cast(unsigned, v); auto rr = __builtin_amdgcn_permlane32_swap(u, u, false, false); return __builtin_bit_cast(float, (unsigned)rr[0]) + __builtin_bit_cast(float, (unsigned)rr[1]); }
; __device__ __forceinline__ float fast_sigmoid(float x) { return __builtin_amdgcn_rcpf(1.f + __builtin_amdgcn_exp2f(-LOG2E * x)); }
; __device__ __forceinline__ u32x4 pack8(const f32x4 a, const f32x4 b) { u32x4 w; w.x = cvt_pk_bf16(a[0], a[1]); w.y = cvt_pk_bf16(a[2], a[3]); w.z = cvt_pk_bf16(b[0], b[1]); w.w = cvt_pk_bf16(b[2], b[3]); return w; }
;     __device__ __forceinline__ void operator()(const f32x4 (&acc)[2][2][4][2], const Unit& u, int wr, int wc, int fr, int fq) const {
;     ...
;             for (int m = mb; m < mb + MBAT; ++m) { const int row = EPI_ROWS(ai, m); const float rs = rs4[m]; float ss = 0.f;
; #pragma unroll
;                 for (int bj = 0; bj < 2; ++bj) { const size_t off = (size_t)row * DM + u.pn * BM + bj * HALF + wc * 32 + 8 * fq;
;                     f32x4 v0, v1; unpack8(hv[m][bj], v0, v1); const f32x4 a0 = acc[ai][bj][m][0], a1 = acc[ai][bj][m][1];
;                     if (MODE == 0) { v0 = v0 + a0 * ascale; v1 = v1 + a1 * ascale; }
;                     else { f32x4 p0, p1; unpack8(pv[m][bj], p0, p1);
; #pragma unroll
;                         for (int e = 0; e < 4; ++e) { v0[e] += fast_sigmoid(a0[e] * rs) * p0[e]; v1[e] += fast_sigmoid(a1[e] * rs) * p1[e]; } }
;                     if (outf) { *(f32x4*)(outf + off) = v0; *(f32x4*)(outf + off + 4) = v1; }
;                     else *(u32x4*)(hout + off) = pack8(v0, v1);
;                     if (h8) { u32x2 w8; w8.x = pk4_fp8(v0[0], v0[1], v0[2], v0[3]); w8.y = pk4_fp8(v1[0], v1[1], v1[2], v1[3]); *(u32x2*)(h8 + off) = w8; }
;                     ss += ((v0[0] * v0[0] + v0[1] * v0[1]) + (v0[2] * v0[2] + v0[3] * v0[3])) + ((v1[0] * v1[0] + v1[1] * v1[1]) + (v1[2] * v1[2] + v1[3] * v1[3])); }
;                 ss += swz_f<16>(ss); ss = sum_x32(ss);
;                 if (fq == 0) ssq_out[(size_t)row * 16 + u.pn * 4 + wc] = ss; }
	s_nop 1
	v_permlane32_swap_b32_e32 v128, v129
	v_fmac_f32_e32 v133, v88, v137
	v_mul_f32_e32 v88, v91, v130
	v_mul_f32_e32 v88, 0xbfb8aa3b, v88
	v_exp_f32_e32 v88, v88
	v_cvt_pk_bf16_f32 v91, v140, v133
	v_cvt_pk_bf16_f32 v92, v141, v134
	s_nop 0
	v_add_f32_e32 v88, 1.0, v88
	v_rcp_f32_e32 v88, v88
	s_nop 0
	v_fmac_f32_e32 v135, v88, v139
	v_lshl_add_u64 v[88:89], v[94:95], 1, s[10:11]
	v_cvt_pk_bf16_f32 v93, v142, v135
	global_store_dwordx4 v[88:89], v[90:93], off
	v_med3_f32 v136, v135, s49, v254
	s_nop 0
	v_med3_f32 v90, v131, s49, v254
	v_med3_f32 v91, v132, s49, v254
	v_cvt_pk_fp8_f32 v90, v90, v91
	v_med3_f32 v92, v140, s49, v254
	v_med3_f32 v93, v133, s49, v254
	v_med3_f32 v91, v141, s49, v254
	v_cvt_pk_fp8_f32 v90, v92, v93 op_sel:[0,0,1]
	v_med3_f32 v92, v134, s49, v254
	v_cvt_pk_fp8_f32 v91, v91, v92
	v_med3_f32 v93, v142, s49, v254
	v_cvt_pk_fp8_f32 v91, v93, v136 op_sel:[0,0,1]
	v_lshl_add_u64 v[92:93], s[18:19], 0, v[94:95]
	v_lshlrev_b32_e32 v95, 16, v118
	v_and_b32_e32 v94, 0xffff0000, v117
	global_store_dwordx2 v[92:93], v[90:91], off
	v_mul_f32_e32 v90, v132, v132
	v_lshlrev_b32_e32 v132, 16, v114
	v_fmac_f32_e32 v95, v80, v132
	v_mul_f32_e32 v80, v85, v130
	v_mul_f32_e32 v80, 0xbfb8aa3b, v80
	v_exp_f32_e32 v80, v80
	v_mul_f32_e32 v91, v133, v133
	v_fmac_f32_e32 v90, v131, v131
	v_fmac_f32_e32 v91, v140, v140
	v_add_f32_e32 v80, 1.0, v80
	v_add_f32_e32 v90, v90, v91
	v_mul_f32_e32 v91, v134, v134
	v_mul_f32_e32 v92, v135, v135
	v_rcp_f32_e32 v80, v80
	v_fmac_f32_e32 v91, v141, v141
	v_fmac_f32_e32 v92, v142, v142
	v_add_f32_e32 v91, v91, v92
	v_add_f32_e32 v90, v90, v91
	v_lshlrev_b32_e32 v91, 16, v116
	v_and_b32_e32 v92, 0xffff0000, v116
	v_lshlrev_b32_e32 v93, 16, v117
	v_and_b32_e32 v116, 0xffff0000, v118
	v_lshlrev_b32_e32 v117, 16, v119
	v_and_b32_e32 v118, 0xffff0000, v119
	v_lshlrev_b32_e32 v119, 16, v112
	v_and_b32_e32 v112, 0xffff0000, v112
	v_fmac_f32_e32 v92, v80, v112
	v_mul_f32_e32 v80, v81, v130
	v_mul_f32_e32 v80, 0xbfb8aa3b, v80
	v_exp_f32_e32 v80, v80
	v_and_b32_e32 v114, 0xffff0000, v114
	v_lshlrev_b32_e32 v131, 16, v113
	v_lshlrev_b32_e32 v133, 16, v115
	v_add_f32_e32 v80, 1.0, v80
	v_rcp_f32_e32 v80, v80
	v_and_b32_e32 v113, 0xffff0000, v113
	v_and_b32_e32 v115, 0xffff0000, v115
	v_fmac_f32_e32 v91, v84, v119
	v_fmac_f32_e32 v116, v80, v114
	v_mul_f32_e32 v80, v86, v130
	v_mul_f32_e32 v80, 0xbfb8aa3b, v80
	v_exp_f32_e32 v80, v80
	s_nop 0
	v_add_f32_e32 v80, 1.0, v80
	v_rcp_f32_e32 v80, v80
	s_nop 0
	v_fmac_f32_e32 v93, v80, v131
	v_mul_f32_e32 v80, v82, v130
	v_mul_f32_e32 v80, 0xbfb8aa3b, v80
	v_exp_f32_e32 v80, v80
	s_nop 0
	v_add_f32_e32 v80, 1.0, v80
	v_rcp_f32_e32 v80, v80
	s_nop 0
	v_fmac_f32_e32 v117, v80, v133
	v_mul_f32_e32 v80, v87, v130
	v_mul_f32_e32 v80, 0xbfb8aa3b, v80
	v_exp_f32_e32 v80, v80
	s_nop 0
	v_add_f32_e32 v80, 1.0, v80
	v_rcp_f32_e32 v80, v80
	s_nop 0
	v_fmac_f32_e32 v94, v80, v113
	v_mul_f32_e32 v80, v83, v130
	v_mul_f32_e32 v80, 0xbfb8aa3b, v80
	v_exp_f32_e32 v80, v80
	s_nop 0
	v_add_f32_e32 v80, 1.0, v80
	v_rcp_f32_e32 v80, v80
	s_nop 0
	v_fmac_f32_e32 v118, v80, v115
	v_cvt_pk_bf16_f32 v80, v91, v92
	v_cvt_pk_bf16_f32 v81, v93, v94
	v_cvt_pk_bf16_f32 v82, v95, v116
	v_cvt_pk_bf16_f32 v83, v117, v118
	global_store_dwordx4 v[88:89], v[80:83], off offset:256
	v_med3_f32 v84, v118, s49, v254
	s_nop 0
	v_med3_f32 v80, v91, s49, v254
	v_med3_f32 v81, v92, s49, v254
	v_cvt_pk_fp8_f32 v80, v80, v81
	v_med3_f32 v82, v93, s49, v254
	v_med3_f32 v83, v94, s49, v254
	v_med3_f32 v81, v95, s49, v254
	v_cvt_pk_fp8_f32 v80, v82, v83 op_sel:[0,0,1]
	v_med3_f32 v82, v116, s49, v254
	v_cvt_pk_fp8_f32 v81, v81, v82
	v_med3_f32 v83, v117, s49, v254
	v_cvt_pk_fp8_f32 v81, v83, v84 op_sel:[0,0,1]
	v_lshl_add_u64 v[82:83], s[28:29], 0, v[126:127]
	global_store_dwordx2 v[82:83], v[80:81], off
	v_mul_f32_e32 v80, v92, v92
	v_mul_f32_e32 v81, v94, v94
	v_fmac_f32_e32 v80, v91, v91
	v_fmac_f32_e32 v81, v93, v93
	v_add_f32_e32 v80, v80, v81
	v_mul_f32_e32 v81, v116, v116
	v_mul_f32_e32 v82, v118, v118
	v_fmac_f32_e32 v81, v95, v95
	v_fmac_f32_e32 v82, v117, v117
	v_add_f32_e32 v81, v81, v82
	v_add_f32_e32 v80, v80, v81
	v_add_f32_e32 v80, v90, v80
	ds_swizzle_b32 v81, v80 offset:swizzle(SWAP,16)
	s_waitcnt lgkmcnt(0)
	v_add_f32_e32 v80, v80, v81
	v_mov_b32_e32 v81, v80
	s_nop 1
	v_permlane32_swap_b32_e32 v80, v81
	s_and_saveexec_b64 s[28:29], vcc
	s_cbranch_execz .LBB0_1953
	s_lshl_b32 s54, s31, 2
	v_add_f32_e32 v82, v80, v81
	s_ashr_i32 s55, s54, 31
	v_lshl_add_u64 v[80:81], s[12:13], 0, v[122:123]
	v_lshl_add_u64 v[80:81], s[54:55], 2, v[80:81]
	s_lshl_b32 s54, s59, 2
	s_mov_b32 s55, s40
	v_lshl_add_u64 v[80:81], v[80:81], 0, s[54:55]
	global_store_dword v[80:81], v82, off
; template <int MASK> __device__ __forceinline__ float swz_f(float v) { return __builtin_bit_cast(float, __builtin_amdgcn_ds_swizzle(__builtin_bit_cast(int, v), (MASK << 10) | 0x1f)); }
; __device__ __forceinline__ float sum_x32(float v) { const unsigned u = __builtin_bit_cast(unsigned, v); auto rr = __builtin_amdgcn_permlane32_swap(u, u, false, false); return __builtin_bit_cast(float, (unsigned)rr[0]) + __builtin_bit_cast(float, (unsigned)rr[1]); }
; __device__ __forceinline__ float fast_sigmoid(float x) { return __builtin_amdgcn_rcpf(1.f + __builtin_amdgcn_exp2f(-LOG2E * x)); }
; __device__ __forceinline__ u32x4 pack8(const f32x4 a, const f32x4 b) { u32x4 w; w.x = cvt_pk_bf16(a[0], a[1]); w.y = cvt_pk_bf16(a[2], a[3]); w.z = cvt_pk_bf16(b[0], b[1]); w.w = cvt_pk_bf16(b[2], b[3]); return w; }
;     __device__ __forceinline__ void operator()(const f32x4 (&acc)[2][2][4][2], const Unit& u, int wr, int wc, int fr, int fq) const {
;     ...
;             for (int m = mb; m < mb + MBAT; ++m) { const int row = EPI_ROWS(ai, m); const float rs = rs4[m]; float ss = 0.f;
; #pragma unroll
;                 for (int bj = 0; bj < 2; ++bj) { const size_t off = (size_t)row * DM + u.pn * BM + bj * HALF + wc * 32 + 8 * fq;
;                     f32x4 v0, v1; unpack8(hv[m][bj], v0, v1); const f32x4 a0 = acc[ai][bj][m][0], a1 = acc[ai][bj][m][1];
;                     if (MODE == 0) { v0 = v0 + a0 * ascale; v1 = v1 + a1 * ascale; }
;                     else { f32x4 p0, p1; unpack8(pv[m][bj], p0, p1);
; #pragma unroll
;                         for (int e = 0; e < 4; ++e) { v0[e] += fast_sigmoid(a0[e] * rs) * p0[e]; v1[e] += fast_sigmoid(a1[e] * rs) * p1[e]; } }
;                     if (outf) { *(f32x4*)(outf + off) = v0; *(f32x4*)(outf + off + 4) = v1; }
;                     else *(u32x4*)(hout + off) = pack8(v0, v1);
;                     if (h8) { u32x2 w8; w8.x = pk4_fp8(v0[0], v0[1], v0[2], v0[3]); w8.y = pk4_fp8(v1[0], v1[1], v1[2], v1[3]); *(u32x2*)(h8 + off) = w8; }
;                     ss += ((v0[0] * v0[0] + v0[1] * v0[1]) + (v0[2] * v0[2] + v0[3] * v0[3])) + ((v1[0] * v1[0] + v1[1] * v1[1]) + (v1[2] * v1[2] + v1[3] * v1[3])); }
;                 ss += swz_f<16>(ss); ss = sum_x32(ss);
;                 if (fq == 0) ssq_out[(size_t)row * 16 + u.pn * 4 + wc] = ss; }
.LBB0_1953:
	s_or_b64 exec, exec, s[28:29]
	v_add_f32_e32 v80, v128, v129
	v_fmamk_f32 v80, v80, 0x3a800000, v230
	v_rsq_f32_e32 v84, v80
	s_nop 0
	v_lshlrev_b32_e32 v89, 16, v110
	s_nop 0
	v_lshlrev_b32_e32 v95, 16, v106
	v_and_b32_e32 v90, 0xffff0000, v110
	v_mul_f32_e32 v72, v72, v84
	v_mul_f32_e32 v72, 0xbfb8aa3b, v72
	v_exp_f32_e32 v72, v72
	v_mul_f32_e32 v73, v73, v84
	v_mul_f32_e32 v73, 0xbfb8aa3b, v73
	v_exp_f32_e32 v73, v73
	v_add_f32_e32 v72, 1.0, v72
	v_rcp_f32_e32 v72, v72
	v_mul_f32_e32 v74, v74, v84
	v_mul_f32_e32 v74, 0xbfb8aa3b, v74
	v_mul_f32_e32 v76, v76, v84
	v_fmac_f32_e32 v89, v72, v95
	v_add_f32_e32 v72, 1.0, v73
	v_mul_f32_e32 v73, v78, v84
	v_mul_f32_e32 v73, 0xbfb8aa3b, v73
	v_mul_f32_e32 v77, v77, v84
	v_rcp_f32_e32 v72, v72
	v_exp_f32_e32 v73, v73
	v_exp_f32_e32 v74, v74
	v_mul_f32_e32 v76, 0xbfb8aa3b, v76
	v_mul_f32_e32 v77, 0xbfb8aa3b, v77
	v_exp_f32_e32 v76, v76
	v_exp_f32_e32 v77, v77
	v_lshlrev_b32_e32 v82, 16, v104
	v_and_b32_e32 v83, 0xffff0000, v104
	v_and_b32_e32 v104, 0xffff0000, v106
	v_fmac_f32_e32 v90, v72, v104
	v_add_f32_e32 v72, 1.0, v73
	v_add_f32_e32 v73, 1.0, v74
	v_mul_f32_e32 v74, v79, v84
	v_mul_f32_e32 v74, 0xbfb8aa3b, v74
	v_mul_f32_e32 v75, v75, v84
	v_add_f32_e32 v76, 1.0, v76
	v_add_f32_e32 v77, 1.0, v77
	v_exp_f32_e32 v74, v74
	v_mul_f32_e32 v75, 0xbfb8aa3b, v75
	v_rcp_f32_e32 v76, v76
	v_rcp_f32_e32 v77, v77
	v_exp_f32_e32 v75, v75
	v_rcp_f32_e32 v72, v72
	v_lshlrev_b32_e32 v85, 16, v108
	v_and_b32_e32 v86, 0xffff0000, v108
	v_add_f32_e32 v74, 1.0, v74
	v_fmac_f32_e32 v85, v76, v82
	v_fmac_f32_e32 v86, v77, v83
	v_rcp_f32_e32 v74, v74
	v_add_f32_e32 v75, 1.0, v75
	v_lshlrev_b32_e32 v87, 16, v109
	v_lshlrev_b32_e32 v93, 16, v105
	v_rcp_f32_e32 v73, v73
	v_rcp_f32_e32 v75, v75
	v_med3_f32 v78, v85, s49, v254
	v_med3_f32 v79, v86, s49, v254
	v_fmac_f32_e32 v87, v72, v93
	v_cvt_pk_fp8_f32 v78, v78, v79
	v_med3_f32 v79, v89, s49, v254
	v_med3_f32 v93, v90, s49, v254
	v_and_b32_e32 v88, 0xffff0000, v109
	v_and_b32_e32 v94, 0xffff0000, v105
	v_cvt_pk_fp8_f32 v79, v79, v93
	v_mul_f32_e32 v64, v64, v84
	v_lshlrev_b32_e32 v91, 16, v111
	v_and_b32_e32 v92, 0xffff0000, v111
	v_lshlrev_b32_e32 v105, 16, v107
	v_and_b32_e32 v106, 0xffff0000, v107
	v_fmac_f32_e32 v88, v74, v94
	v_mul_f32_e32 v64, 0xbfb8aa3b, v64
	v_fmac_f32_e32 v91, v73, v105
	v_fmac_f32_e32 v92, v75, v106
	v_med3_f32 v82, v87, s49, v254
	v_med3_f32 v83, v88, s49, v254
	v_exp_f32_e32 v64, v64
	v_cvt_pk_fp8_f32 v78, v82, v83 op_sel:[0,0,1]
	v_med3_f32 v82, v91, s49, v254
	v_med3_f32 v83, v92, s49, v254
	v_lshl_add_u64 v[80:81], v[124:125], 0, v[152:153]
	v_cvt_pk_fp8_f32 v79, v82, v83 op_sel:[0,0,1]
	v_lshl_add_u64 v[76:77], v[80:81], 0, s[6:7]
	v_mul_f32_e32 v65, v65, v84
	v_cvt_pk_bf16_f32 v72, v85, v86
	v_cvt_pk_bf16_f32 v73, v87, v88
	v_lshl_add_u64 v[82:83], v[76:77], 1, s[10:11]
	v_add_f32_e32 v64, 1.0, v64
	v_mul_f32_e32 v65, 0xbfb8aa3b, v65
	v_cvt_pk_bf16_f32 v74, v89, v90
	v_cvt_pk_bf16_f32 v75, v91, v92
	global_store_dwordx4 v[82:83], v[72:75], off
	v_rcp_f32_e32 v64, v64
	v_exp_f32_e32 v65, v65
	v_lshl_add_u64 v[72:73], s[18:19], 0, v[76:77]
	global_store_dwordx2 v[72:73], v[78:79], off
	v_mul_f32_e32 v72, v86, v86
	v_mul_f32_e32 v73, v88, v88
	v_fmac_f32_e32 v72, v85, v85
	v_fmac_f32_e32 v73, v87, v87
	v_add_f32_e32 v72, v72, v73
	v_mul_f32_e32 v73, v90, v90
	s_nop 0
	v_lshlrev_b32_e32 v77, 16, v102
	s_nop 0
	v_lshlrev_b32_e32 v90, 16, v98
	v_fmac_f32_e32 v77, v64, v90
	v_add_f32_e32 v64, 1.0, v65
	v_mul_f32_e32 v65, v70, v84
	v_mul_f32_e32 v66, v66, v84
	v_mul_f32_e32 v65, 0xbfb8aa3b, v65
	v_mul_f32_e32 v66, 0xbfb8aa3b, v66
	v_rcp_f32_e32 v64, v64
	v_exp_f32_e32 v65, v65
	v_exp_f32_e32 v66, v66
	v_mul_f32_e32 v74, v92, v92
	v_fmac_f32_e32 v74, v91, v91
	v_and_b32_e32 v78, 0xffff0000, v102
	v_and_b32_e32 v91, 0xffff0000, v98
	v_mul_f32_e32 v68, v68, v84
	v_mul_f32_e32 v69, v69, v84
	v_fmac_f32_e32 v78, v64, v91
	v_add_f32_e32 v64, 1.0, v65
	v_add_f32_e32 v65, 1.0, v66
	v_mul_f32_e32 v66, v71, v84
	v_mul_f32_e32 v68, 0xbfb8aa3b, v68
	v_mul_f32_e32 v69, 0xbfb8aa3b, v69
	v_mul_f32_e32 v66, 0xbfb8aa3b, v66
	v_mul_f32_e32 v67, v67, v84
	v_exp_f32_e32 v68, v68
	v_exp_f32_e32 v69, v69
	v_exp_f32_e32 v66, v66
	v_mul_f32_e32 v67, 0xbfb8aa3b, v67
	v_exp_f32_e32 v67, v67
	v_add_f32_e32 v68, 1.0, v68
	v_add_f32_e32 v69, 1.0, v69
	v_add_f32_e32 v66, 1.0, v66
	v_rcp_f32_e32 v68, v68
	v_rcp_f32_e32 v69, v69
	v_rcp_f32_e32 v64, v64
	v_rcp_f32_e32 v65, v65
	v_rcp_f32_e32 v66, v66
	v_add_f32_e32 v67, 1.0, v67
	v_fmac_f32_e32 v73, v89, v89
	v_rcp_f32_e32 v67, v67
	v_add_f32_e32 v73, v73, v74
	v_add_f32_e32 v72, v72, v73
	v_lshlrev_b32_e32 v73, 16, v100
	v_and_b32_e32 v74, 0xffff0000, v100
	v_lshlrev_b32_e32 v75, 16, v101
	v_and_b32_e32 v76, 0xffff0000, v101
	v_lshlrev_b32_e32 v79, 16, v103
	v_lshlrev_b32_e32 v86, 16, v96
	v_and_b32_e32 v87, 0xffff0000, v96
	v_lshlrev_b32_e32 v88, 16, v97
	v_and_b32_e32 v89, 0xffff0000, v97
	v_lshlrev_b32_e32 v92, 16, v99
	v_and_b32_e32 v85, 0xffff0000, v103
	v_and_b32_e32 v93, 0xffff0000, v99
	v_fmac_f32_e32 v73, v68, v86
	v_fmac_f32_e32 v74, v69, v87
	v_fmac_f32_e32 v75, v64, v88
	v_fmac_f32_e32 v79, v65, v92
	v_fmac_f32_e32 v76, v66, v89
	v_cvt_pk_bf16_f32 v64, v73, v74
	v_cvt_pk_bf16_f32 v65, v75, v76
	v_fmac_f32_e32 v85, v67, v93
	v_cvt_pk_bf16_f32 v66, v77, v78
	v_cvt_pk_bf16_f32 v67, v79, v85
	global_store_dwordx4 v[82:83], v[64:67], off offset:256
	v_med3_f32 v68, v78, s49, v254
	s_add_u32 s28, s18, s95
	v_med3_f32 v64, v73, s49, v254
	v_med3_f32 v65, v74, s49, v254
	v_cvt_pk_fp8_f32 v64, v64, v65
	v_med3_f32 v65, v77, s49, v254
	v_cvt_pk_fp8_f32 v65, v65, v68
	v_med3_f32 v66, v75, s49, v254
	v_med3_f32 v67, v76, s49, v254
	v_cvt_pk_fp8_f32 v64, v66, v67 op_sel:[0,0,1]
	v_med3_f32 v66, v79, s49, v254
	v_med3_f32 v67, v85, s49, v254
	v_cvt_pk_fp8_f32 v65, v66, v67 op_sel:[0,0,1]
	v_mul_f32_e32 v66, v74, v74
	v_mul_f32_e32 v67, v76, v76
	v_fmac_f32_e32 v66, v73, v73
	v_fmac_f32_e32 v67, v75, v75
	v_add_f32_e32 v66, v66, v67
	v_mul_f32_e32 v67, v78, v78
	v_mul_f32_e32 v68, v85, v85
	v_fmac_f32_e32 v67, v77, v77
	v_fmac_f32_e32 v68, v79, v79
	v_add_f32_e32 v67, v67, v68
	v_add_f32_e32 v66, v66, v67
	v_add_f32_e32 v68, v72, v66
	ds_swizzle_b32 v69, v68 offset:swizzle(SWAP,16)
	s_addc_u32 s29, s19, s96
	v_lshl_add_u64 v[66:67], s[28:29], 0, v[80:81]
	global_store_dwordx2 v[66:67], v[64:65], off
	s_waitcnt lgkmcnt(0)
	v_add_f32_e32 v64, v68, v69
	v_mov_b32_e32 v65, v64
	s_nop 1
	v_permlane32_swap_b32_e32 v64, v65
	s_and_saveexec_b64 s[28:29], vcc
	s_cbranch_execz .LBB0_1955
	s_lshl_b32 s54, s31, 2
	v_add_f32_e32 v66, v64, v65
	s_ashr_i32 s55, s54, 31
	v_lshl_add_u64 v[64:65], s[12:13], 0, v[120:121]
	v_lshl_add_u64 v[64:65], s[54:55], 2, v[64:65]
	s_lshl_b32 s54, s59, 2
	s_mov_b32 s55, s40
	v_lshl_add_u64 v[64:65], v[64:65], 0, s[54:55]
	global_store_dword v[64:65], v66, off
; __device__ __forceinline__ float fast_sigmoid(float x) { return __builtin_amdgcn_rcpf(1.f + __builtin_amdgcn_exp2f(-LOG2E * x)); }
;     __device__ __forceinline__ void operator()(const f32x4 (&acc)[2][2][4][2], const Unit& u, int wr, int wc, int fr, int fq) const {
;     ...
;         for (int mb = 0; mb < 4; mb += MBAT) {
;             u32x4 hv[4][2], pv[4][2]; float rs4[4];
; #pragma unroll
;             for (int m = mb; m < mb + MBAT; ++m) { const int row = EPI_ROWS(ai, m); rs4[m] = 0.f; if (MODE == 1) rs4[m] = rstd_q(ssq_in, row, fq) * ascale;
; #pragma unroll
;                 for (int bj = 0; bj < 2; ++bj) { const size_t off = (size_t)row * DM + u.pn * BM + bj * HALF + wc * 32 + 8 * fq; hv[m][bj] = *(const u32x4*)(hin + off); if (MODE == 1) pv[m][bj] = *(const u32x4*)(PP + off); } }
; #pragma unroll
;             for (int m = mb; m < mb + MBAT; ++m) { const int row = EPI_ROWS(ai, m); const float rs = rs4[m]; float ss = 0.f;
; #pragma unroll
;                 for (int bj = 0; bj < 2; ++bj) { const size_t off = (size_t)row * DM + u.pn * BM + bj * HALF + wc * 32 + 8 * fq;
;                     f32x4 v0, v1; unpack8(hv[m][bj], v0, v1); const f32x4 a0 = acc[ai][bj][m][0], a1 = acc[ai][bj][m][1];
;                     if (MODE == 0) { v0 = v0 + a0 * ascale; v1 = v1 + a1 * ascale; }
;                     else { f32x4 p0, p1; unpack8(pv[m][bj], p0, p1);
; #pragma unroll
;                         for (int e = 0; e < 4; ++e) { v0[e] += fast_sigmoid(a0[e] * rs) * p0[e]; v1[e] += fast_sigmoid(a1[e] * rs) * p1[e]; } }
.LBB0_1955:
	s_or_b64 exec, exec, s[28:29]
	v_add_u32_e32 v68, 0x80, v158
	v_ashrrev_i32_e32 v69, 31, v68
	v_lshlrev_b64 v[90:91], 6, v[68:69]
	v_lshl_add_u64 v[64:65], v[156:157], 0, v[90:91]
	s_nop 0
	v_lshlrev_b64 v[94:95], 10, v[68:69]
	v_add_u32_e32 v68, 0x90, v158
	v_ashrrev_i32_e32 v69, 31, v68
	v_lshlrev_b64 v[88:89], 6, v[68:69]
	v_lshlrev_b64 v[92:93], 10, v[68:69]
	s_add_u32 s28, s18, s95
	s_addc_u32 s29, s19, s96
	s_waitcnt vmcnt(8)
	v_mov_b32_e32 v64, v200
	v_mov_b32_e32 v65, v201
	v_mov_b32_e32 v66, v202
	v_mov_b32_e32 v67, v203
	v_add_f32_e32 v64, v64, v65
	v_add_f32_e32 v65, v66, v67
	v_add_f32_e32 v64, v64, v65
	ds_swizzle_b32 v65, v64 offset:swizzle(SWAP,16)
	s_waitcnt lgkmcnt(0)
	v_add_f32_e32 v64, v64, v65
	v_mov_b32_e32 v65, v64
	s_nop 1
	v_permlane32_swap_b32_e32 v64, v65
	v_add_f32_e32 v64, v64, v65
	v_fmamk_f32 v64, v64, 0x3a800000, v230
	v_rsq_f32_e32 v98, v64
	v_lshl_add_u64 v[64:65], v[94:95], 0, v[154:155]
	v_lshlrev_b64 v[64:65], 1, v[64:65]
	v_lshl_add_u64 v[66:67], s[2:3], 0, v[64:65]
	v_mov_b32_e32 v100, v204
	v_mov_b32_e32 v101, v205
	v_mov_b32_e32 v102, v206
	v_mov_b32_e32 v103, v207
	v_lshl_add_u64 v[64:65], s[14:15], 0, v[64:65]
	v_mov_b32_e32 v104, v208
	v_mov_b32_e32 v105, v209
	v_mov_b32_e32 v106, v210
	v_mov_b32_e32 v107, v211
	v_mov_b32_e32 v84, v212
	v_mov_b32_e32 v85, v213
	v_mov_b32_e32 v86, v214
	v_mov_b32_e32 v87, v215
	v_mov_b32_e32 v80, v216
	v_mov_b32_e32 v81, v217
	v_mov_b32_e32 v82, v218
	v_mov_b32_e32 v83, v219
	v_lshl_add_u64 v[64:65], v[156:157], 0, v[88:89]
	v_mov_b32_e32 v64, v220
	v_mov_b32_e32 v65, v221
	v_mov_b32_e32 v66, v222
	v_mov_b32_e32 v67, v223
	v_mul_f32_e32 v56, v56, v98
	v_mul_f32_e32 v56, 0xbfb8aa3b, v56
	v_exp_f32_e32 v56, v56
	v_mul_f32_e32 v60, v60, v98
	v_mul_f32_e32 v60, 0xbfb8aa3b, v60
	v_exp_f32_e32 v60, v60
	v_add_f32_e32 v56, 1.0, v56
	v_rcp_f32_e32 v56, v56
	v_lshl_add_u64 v[94:95], v[94:95], 0, v[152:153]
	v_add_f32_e32 v60, 1.0, v60
	v_rcp_f32_e32 v60, v60
	v_mul_f32_e32 v48, v48, v98
	v_mul_f32_e32 v48, 0xbfb8aa3b, v48
	v_exp_f32_e32 v48, v48
	v_mul_f32_e32 v52, v52, v98
	v_mul_f32_e32 v52, 0xbfb8aa3b, v52
	v_exp_f32_e32 v52, v52
	v_add_f32_e32 v48, 1.0, v48
	v_rcp_f32_e32 v48, v48
	v_add_f32_e32 v52, 1.0, v52
	v_rcp_f32_e32 v52, v52
	s_nop 0
	v_lshlrev_b32_e32 v113, 16, v106
	v_lshlrev_b32_e32 v109, 16, v102
	v_fmac_f32_e32 v109, v56, v113
	v_mul_f32_e32 v56, v61, v98
	v_mul_f32_e32 v56, 0xbfb8aa3b, v56
	v_exp_f32_e32 v56, v56
	v_lshlrev_b32_e32 v99, 16, v100
	v_and_b32_e32 v100, 0xffff0000, v100
	v_lshlrev_b32_e32 v111, 16, v104
	v_add_f32_e32 v56, 1.0, v56
	v_rcp_f32_e32 v56, v56
	v_and_b32_e32 v104, 0xffff0000, v104
	v_and_b32_e32 v102, 0xffff0000, v102
	v_and_b32_e32 v106, 0xffff0000, v106
	v_fmac_f32_e32 v100, v56, v104
	v_mul_f32_e32 v56, v57, v98
	v_mul_f32_e32 v56, 0xbfb8aa3b, v56
	v_exp_f32_e32 v56, v56
	v_lshlrev_b32_e32 v108, 16, v101
	v_lshlrev_b32_e32 v112, 16, v105
	v_lshlrev_b32_e32 v110, 16, v103
	v_add_f32_e32 v56, 1.0, v56
	v_rcp_f32_e32 v56, v56
	v_lshlrev_b32_e32 v114, 16, v107
	v_and_b32_e32 v101, 0xffff0000, v101
	v_and_b32_e32 v105, 0xffff0000, v105
	v_fmac_f32_e32 v102, v56, v106
	v_mul_f32_e32 v56, v62, v98
	v_mul_f32_e32 v56, 0xbfb8aa3b, v56
	v_exp_f32_e32 v56, v56
	s_nop 0
	v_add_f32_e32 v64, v64, v65
	v_add_f32_e32 v65, v66, v67
	v_add_f32_e32 v64, v64, v65
	v_add_f32_e32 v56, 1.0, v56
	v_rcp_f32_e32 v56, v56
	ds_swizzle_b32 v65, v64 offset:swizzle(SWAP,16)
	v_and_b32_e32 v103, 0xffff0000, v103
	v_and_b32_e32 v107, 0xffff0000, v107
	v_fmac_f32_e32 v108, v56, v112
	v_mul_f32_e32 v56, v58, v98
	v_mul_f32_e32 v56, 0xbfb8aa3b, v56
	v_exp_f32_e32 v56, v56
	s_waitcnt lgkmcnt(0)
	v_add_f32_e32 v96, v64, v65
	v_lshl_add_u64 v[64:65], v[92:93], 0, v[154:155]
	v_lshlrev_b64 v[64:65], 1, v[64:65]
	v_add_f32_e32 v56, 1.0, v56
	v_rcp_f32_e32 v56, v56
	v_lshl_add_u64 v[66:67], s[2:3], 0, v[64:65]
	v_lshl_add_u64 v[64:65], s[14:15], 0, v[64:65]
	v_mov_b32_e32 v76, v236
	v_mov_b32_e32 v77, v237
	v_mov_b32_e32 v78, v238
	v_mov_b32_e32 v79, v239
	v_fmac_f32_e32 v110, v56, v114
	v_mul_f32_e32 v56, v63, v98
	v_mul_f32_e32 v56, 0xbfb8aa3b, v56
	v_exp_f32_e32 v56, v56
	v_lshl_add_u64 v[62:63], v[94:95], 0, s[6:7]
	v_mov_b32_e32 v72, v240
	v_mov_b32_e32 v73, v241
	v_mov_b32_e32 v74, v242
	v_mov_b32_e32 v75, v243
	v_mov_b32_e32 v68, v244
	v_mov_b32_e32 v69, v245
	v_mov_b32_e32 v70, v246
	v_mov_b32_e32 v71, v247
	s_nop 0
	v_mov_b32_e32 v64, v248
	v_mov_b32_e32 v65, v249
	v_mov_b32_e32 v66, v250
	v_mov_b32_e32 v67, v251
	v_add_u32_e32 v228, 0x2800, v227
	v_add_u32_e32 v229, 0x50000, v226
	global_load_dwordx4 v[200:203], v228, s[16:17]
	global_load_dwordx4 v[204:207], v229, s[2:3]
	global_load_dwordx4 v[208:211], v229, s[14:15]
	global_load_dwordx4 v[212:215], v229, s[2:3] offset:256
	global_load_dwordx4 v[216:219], v229, s[14:15] offset:256
	global_load_dwordx4 v[220:223], v228, s[16:17] offset:1024
	v_add_u32_e32 v225, 0x58000, v226
	global_load_dwordx4 v[236:239], v225, s[2:3]
	global_load_dwordx4 v[240:243], v225, s[14:15]
	global_load_dwordx4 v[244:247], v225, s[2:3] offset:256
	global_load_dwordx4 v[248:251], v225, s[14:15] offset:256
	v_fmac_f32_e32 v99, v60, v111
	v_add_f32_e32 v56, 1.0, v56
	v_rcp_f32_e32 v56, v56
	v_cvt_pk_bf16_f32 v58, v99, v100
	v_mov_b32_e32 v97, v96
	s_nop 1
	v_permlane32_swap_b32_e32 v96, v97
	v_fmac_f32_e32 v101, v56, v105
	v_mul_f32_e32 v56, v59, v98
	v_mul_f32_e32 v56, 0xbfb8aa3b, v56
	v_exp_f32_e32 v56, v56
	v_cvt_pk_bf16_f32 v59, v108, v101
	v_cvt_pk_bf16_f32 v60, v109, v102
	s_nop 0
	v_add_f32_e32 v56, 1.0, v56
	v_rcp_f32_e32 v56, v56
	s_nop 0
	v_fmac_f32_e32 v103, v56, v107
	v_lshl_add_u64 v[56:57], v[62:63], 1, s[10:11]
; template <int MASK> __device__ __forceinline__ float swz_f(float v) { return __builtin_bit_cast(float, __builtin_amdgcn_ds_swizzle(__builtin_bit_cast(int, v), (MASK << 10) | 0x1f)); }
; __device__ __forceinline__ float sum_x32(float v) { const unsigned u = __builtin_bit_cast(unsigned, v); auto rr = __builtin_amdgcn_permlane32_swap(u, u, false, false); return __builtin_bit_cast(float, (unsigned)rr[0]) + __builtin_bit_cast(float, (unsigned)rr[1]); }
; __device__ __forceinline__ float fast_sigmoid(float x) { return __builtin_amdgcn_rcpf(1.f + __builtin_amdgcn_exp2f(-LOG2E * x)); }
; __device__ __forceinline__ u32x4 pack8(const f32x4 a, const f32x4 b) { u32x4 w; w.x = cvt_pk_bf16(a[0], a[1]); w.y = cvt_pk_bf16(a[2], a[3]); w.z = cvt_pk_bf16(b[0], b[1]); w.w = cvt_pk_bf16(b[2], b[3]); return w; }
;     __device__ __forceinline__ void operator()(const f32x4 (&acc)[2][2][4][2], const Unit& u, int wr, int wc, int fr, int fq) const {
;     ...
;             for (int m = mb; m < mb + MBAT; ++m) { const int row = EPI_ROWS(ai, m); const float rs = rs4[m]; float ss = 0.f;
; #pragma unroll
;                 for (int bj = 0; bj < 2; ++bj) { const size_t off = (size_t)row * DM + u.pn * BM + bj * HALF + wc * 32 + 8 * fq;
;                     f32x4 v0, v1; unpack8(hv[m][bj], v0, v1); const f32x4 a0 = acc[ai][bj][m][0], a1 = acc[ai][bj][m][1];
;                     if (MODE == 0) { v0 = v0 + a0 * ascale; v1 = v1 + a1 * ascale; }
;                     else { f32x4 p0, p1; unpack8(pv[m][bj], p0, p1);
; #pragma unroll
;                         for (int e = 0; e < 4; ++e) { v0[e] += fast_sigmoid(a0[e] * rs) * p0[e]; v1[e] += fast_sigmoid(a1[e] * rs) * p1[e]; } }
;                     if (outf) { *(f32x4*)(outf + off) = v0; *(f32x4*)(outf + off + 4) = v1; }
;                     else *(u32x4*)(hout + off) = pack8(v0, v1);
;                     if (h8) { u32x2 w8; w8.x = pk4_fp8(v0[0], v0[1], v0[2], v0[3]); w8.y = pk4_fp8(v1[0], v1[1], v1[2], v1[3]); *(u32x2*)(h8 + off) = w8; }
;                     ss += ((v0[0] * v0[0] + v0[1] * v0[1]) + (v0[2] * v0[2] + v0[3] * v0[3])) + ((v1[0] * v1[0] + v1[1] * v1[1]) + (v1[2] * v1[2] + v1[3] * v1[3])); }
;                 ss += swz_f<16>(ss); ss = sum_x32(ss);
;                 if (fq == 0) ssq_out[(size_t)row * 16 + u.pn * 4 + wc] = ss; }
	v_cvt_pk_bf16_f32 v61, v110, v103
	global_store_dwordx4 v[56:57], v[58:61], off
	v_med3_f32 v104, v103, s49, v254
	s_nop 0
	v_med3_f32 v58, v99, s49, v254
	v_med3_f32 v59, v100, s49, v254
	v_cvt_pk_fp8_f32 v58, v58, v59
	v_med3_f32 v60, v108, s49, v254
	v_med3_f32 v61, v101, s49, v254
	v_med3_f32 v59, v109, s49, v254
	v_cvt_pk_fp8_f32 v58, v60, v61 op_sel:[0,0,1]
	v_med3_f32 v60, v102, s49, v254
	v_cvt_pk_fp8_f32 v59, v59, v60
	v_med3_f32 v61, v110, s49, v254
	v_cvt_pk_fp8_f32 v59, v61, v104 op_sel:[0,0,1]
	v_lshl_add_u64 v[60:61], s[18:19], 0, v[62:63]
	v_lshlrev_b32_e32 v63, 16, v86
	v_and_b32_e32 v62, 0xffff0000, v85
	global_store_dwordx2 v[60:61], v[58:59], off
	v_mul_f32_e32 v58, v100, v100
	v_lshlrev_b32_e32 v100, 16, v82
	v_fmac_f32_e32 v63, v48, v100
	v_mul_f32_e32 v48, v53, v98
	v_mul_f32_e32 v48, 0xbfb8aa3b, v48
	v_exp_f32_e32 v48, v48
	v_mul_f32_e32 v59, v101, v101
	v_fmac_f32_e32 v58, v99, v99
	v_fmac_f32_e32 v59, v108, v108
	v_add_f32_e32 v48, 1.0, v48
	v_add_f32_e32 v58, v58, v59
	v_mul_f32_e32 v59, v102, v102
	v_mul_f32_e32 v60, v103, v103
	v_rcp_f32_e32 v48, v48
	v_fmac_f32_e32 v59, v109, v109
	v_fmac_f32_e32 v60, v110, v110
	v_add_f32_e32 v59, v59, v60
	v_add_f32_e32 v58, v58, v59
	v_lshlrev_b32_e32 v59, 16, v84
	v_and_b32_e32 v60, 0xffff0000, v84
	v_lshlrev_b32_e32 v61, 16, v85
	v_and_b32_e32 v84, 0xffff0000, v86
	v_lshlrev_b32_e32 v85, 16, v87
	v_and_b32_e32 v86, 0xffff0000, v87
	v_lshlrev_b32_e32 v87, 16, v80
	v_and_b32_e32 v80, 0xffff0000, v80
	v_fmac_f32_e32 v60, v48, v80
	v_mul_f32_e32 v48, v49, v98
	v_mul_f32_e32 v48, 0xbfb8aa3b, v48
	v_exp_f32_e32 v48, v48
	v_and_b32_e32 v82, 0xffff0000, v82
	v_lshlrev_b32_e32 v99, 16, v81
	v_lshlrev_b32_e32 v101, 16, v83
	v_add_f32_e32 v48, 1.0, v48
	v_rcp_f32_e32 v48, v48
	v_and_b32_e32 v81, 0xffff0000, v81
	v_and_b32_e32 v83, 0xffff0000, v83
	v_fmac_f32_e32 v59, v52, v87
	v_fmac_f32_e32 v84, v48, v82
	v_mul_f32_e32 v48, v54, v98
	v_mul_f32_e32 v48, 0xbfb8aa3b, v48
	v_exp_f32_e32 v48, v48
	s_nop 0
	v_add_f32_e32 v48, 1.0, v48
	v_rcp_f32_e32 v48, v48
	s_nop 0
	v_fmac_f32_e32 v61, v48, v99
	v_mul_f32_e32 v48, v50, v98
	v_mul_f32_e32 v48, 0xbfb8aa3b, v48
	v_exp_f32_e32 v48, v48
	s_nop 0
	v_add_f32_e32 v48, 1.0, v48
	v_rcp_f32_e32 v48, v48
	s_nop 0
	v_fmac_f32_e32 v85, v48, v101
	v_mul_f32_e32 v48, v55, v98
	v_mul_f32_e32 v48, 0xbfb8aa3b, v48
	v_exp_f32_e32 v48, v48
	s_nop 0
	v_add_f32_e32 v48, 1.0, v48
	v_rcp_f32_e32 v48, v48
	s_nop 0
	v_fmac_f32_e32 v62, v48, v81
	v_mul_f32_e32 v48, v51, v98
	v_mul_f32_e32 v48, 0xbfb8aa3b, v48
	v_exp_f32_e32 v48, v48
	s_nop 0
	v_add_f32_e32 v48, 1.0, v48
	v_rcp_f32_e32 v48, v48
	s_nop 0
	v_fmac_f32_e32 v86, v48, v83
	v_cvt_pk_bf16_f32 v48, v59, v60
	v_cvt_pk_bf16_f32 v49, v61, v62
	v_cvt_pk_bf16_f32 v50, v63, v84
	v_cvt_pk_bf16_f32 v51, v85, v86
	global_store_dwordx4 v[56:57], v[48:51], off offset:256
	v_med3_f32 v52, v86, s49, v254
	s_nop 0
	v_med3_f32 v48, v59, s49, v254
	v_med3_f32 v49, v60, s49, v254
	v_cvt_pk_fp8_f32 v48, v48, v49
	v_med3_f32 v50, v61, s49, v254
	v_med3_f32 v51, v62, s49, v254
	v_med3_f32 v49, v63, s49, v254
	v_cvt_pk_fp8_f32 v48, v50, v51 op_sel:[0,0,1]
	v_med3_f32 v50, v84, s49, v254
	v_cvt_pk_fp8_f32 v49, v49, v50
	v_med3_f32 v51, v85, s49, v254
	v_cvt_pk_fp8_f32 v49, v51, v52 op_sel:[0,0,1]
	v_lshl_add_u64 v[50:51], s[28:29], 0, v[94:95]
	global_store_dwordx2 v[50:51], v[48:49], off
	v_mul_f32_e32 v48, v60, v60
	v_mul_f32_e32 v49, v62, v62
	v_fmac_f32_e32 v48, v59, v59
	v_fmac_f32_e32 v49, v61, v61
	v_add_f32_e32 v48, v48, v49
	v_mul_f32_e32 v49, v84, v84
	v_mul_f32_e32 v50, v86, v86
	v_fmac_f32_e32 v49, v63, v63
	v_fmac_f32_e32 v50, v85, v85
	v_add_f32_e32 v49, v49, v50
	v_add_f32_e32 v48, v48, v49
	v_add_f32_e32 v48, v58, v48
	ds_swizzle_b32 v49, v48 offset:swizzle(SWAP,16)
	s_waitcnt lgkmcnt(0)
	v_add_f32_e32 v48, v48, v49
	v_mov_b32_e32 v49, v48
	s_nop 1
	v_permlane32_swap_b32_e32 v48, v49
	s_and_saveexec_b64 s[28:29], vcc
	s_cbranch_execz .LBB0_1957
	s_lshl_b32 s54, s31, 2
	v_add_f32_e32 v50, v48, v49
	s_ashr_i32 s55, s54, 31
	v_lshl_add_u64 v[48:49], s[12:13], 0, v[90:91]
	v_lshl_add_u64 v[48:49], s[54:55], 2, v[48:49]
	s_lshl_b32 s54, s59, 2
	s_mov_b32 s55, s40
	v_lshl_add_u64 v[48:49], v[48:49], 0, s[54:55]
	global_store_dword v[48:49], v50, off
; template <int MASK> __device__ __forceinline__ float swz_f(float v) { return __builtin_bit_cast(float, __builtin_amdgcn_ds_swizzle(__builtin_bit_cast(int, v), (MASK << 10) | 0x1f)); }
; __device__ __forceinline__ float sum_x32(float v) { const unsigned u = __builtin_bit_cast(unsigned, v); auto rr = __builtin_amdgcn_permlane32_swap(u, u, false, false); return __builtin_bit_cast(float, (unsigned)rr[0]) + __builtin_bit_cast(float, (unsigned)rr[1]); }
; __device__ __forceinline__ float fast_sigmoid(float x) { return __builtin_amdgcn_rcpf(1.f + __builtin_amdgcn_exp2f(-LOG2E * x)); }
; __device__ __forceinline__ u32x4 pack8(const f32x4 a, const f32x4 b) { u32x4 w; w.x = cvt_pk_bf16(a[0], a[1]); w.y = cvt_pk_bf16(a[2], a[3]); w.z = cvt_pk_bf16(b[0], b[1]); w.w = cvt_pk_bf16(b[2], b[3]); return w; }
;     __device__ __forceinline__ void operator()(const f32x4 (&acc)[2][2][4][2], const Unit& u, int wr, int wc, int fr, int fq) const {
;     ...
;             for (int m = mb; m < mb + MBAT; ++m) { const int row = EPI_ROWS(ai, m); const float rs = rs4[m]; float ss = 0.f;
; #pragma unroll
;                 for (int bj = 0; bj < 2; ++bj) { const size_t off = (size_t)row * DM + u.pn * BM + bj * HALF + wc * 32 + 8 * fq;
;                     f32x4 v0, v1; unpack8(hv[m][bj], v0, v1); const f32x4 a0 = acc[ai][bj][m][0], a1 = acc[ai][bj][m][1];
;                     if (MODE == 0) { v0 = v0 + a0 * ascale; v1 = v1 + a1 * ascale; }
;                     else { f32x4 p0, p1; unpack8(pv[m][bj], p0, p1);
; #pragma unroll
;                         for (int e = 0; e < 4; ++e) { v0[e] += fast_sigmoid(a0[e] * rs) * p0[e]; v1[e] += fast_sigmoid(a1[e] * rs) * p1[e]; } }
;                     if (outf) { *(f32x4*)(outf + off) = v0; *(f32x4*)(outf + off + 4) = v1; }
;                     else *(u32x4*)(hout + off) = pack8(v0, v1);
;                     if (h8) { u32x2 w8; w8.x = pk4_fp8(v0[0], v0[1], v0[2], v0[3]); w8.y = pk4_fp8(v1[0], v1[1], v1[2], v1[3]); *(u32x2*)(h8 + off) = w8; }
;                     ss += ((v0[0] * v0[0] + v0[1] * v0[1]) + (v0[2] * v0[2] + v0[3] * v0[3])) + ((v1[0] * v1[0] + v1[1] * v1[1]) + (v1[2] * v1[2] + v1[3] * v1[3])); }
;                 ss += swz_f<16>(ss); ss = sum_x32(ss);
;                 if (fq == 0) ssq_out[(size_t)row * 16 + u.pn * 4 + wc] = ss; }
.LBB0_1957:
	s_or_b64 exec, exec, s[28:29]
	v_add_f32_e32 v48, v96, v97
	v_fmamk_f32 v48, v48, 0x3a800000, v230
	v_rsq_f32_e32 v52, v48
	s_nop 0
	v_lshlrev_b32_e32 v57, 16, v78
	s_nop 0
	v_lshlrev_b32_e32 v63, 16, v74
	v_and_b32_e32 v58, 0xffff0000, v78
	v_mul_f32_e32 v40, v40, v52
	v_mul_f32_e32 v40, 0xbfb8aa3b, v40
	v_exp_f32_e32 v40, v40
	v_mul_f32_e32 v41, v41, v52
	v_mul_f32_e32 v41, 0xbfb8aa3b, v41
	v_exp_f32_e32 v41, v41
	v_add_f32_e32 v40, 1.0, v40
	v_rcp_f32_e32 v40, v40
	v_mul_f32_e32 v42, v42, v52
	v_mul_f32_e32 v42, 0xbfb8aa3b, v42
	v_mul_f32_e32 v44, v44, v52
	v_fmac_f32_e32 v57, v40, v63
	v_add_f32_e32 v40, 1.0, v41
	v_mul_f32_e32 v41, v46, v52
	v_mul_f32_e32 v41, 0xbfb8aa3b, v41
	v_mul_f32_e32 v45, v45, v52
	v_rcp_f32_e32 v40, v40
	v_exp_f32_e32 v41, v41
	v_exp_f32_e32 v42, v42
	v_mul_f32_e32 v44, 0xbfb8aa3b, v44
	v_mul_f32_e32 v45, 0xbfb8aa3b, v45
	v_exp_f32_e32 v44, v44
	v_exp_f32_e32 v45, v45
	v_lshlrev_b32_e32 v50, 16, v72
	v_and_b32_e32 v51, 0xffff0000, v72
	v_and_b32_e32 v72, 0xffff0000, v74
	v_fmac_f32_e32 v58, v40, v72
	v_add_f32_e32 v40, 1.0, v41
	v_add_f32_e32 v41, 1.0, v42
	v_mul_f32_e32 v42, v47, v52
	v_mul_f32_e32 v42, 0xbfb8aa3b, v42
	v_mul_f32_e32 v43, v43, v52
	v_add_f32_e32 v44, 1.0, v44
	v_add_f32_e32 v45, 1.0, v45
	v_exp_f32_e32 v42, v42
	v_mul_f32_e32 v43, 0xbfb8aa3b, v43
	v_rcp_f32_e32 v44, v44
	v_rcp_f32_e32 v45, v45
	v_exp_f32_e32 v43, v43
	v_rcp_f32_e32 v40, v40
	v_lshlrev_b32_e32 v53, 16, v76
	v_and_b32_e32 v54, 0xffff0000, v76
	v_add_f32_e32 v42, 1.0, v42
	v_fmac_f32_e32 v53, v44, v50
	v_fmac_f32_e32 v54, v45, v51
	v_rcp_f32_e32 v42, v42
	v_add_f32_e32 v43, 1.0, v43
	v_lshlrev_b32_e32 v55, 16, v77
	v_lshlrev_b32_e32 v61, 16, v73
	v_rcp_f32_e32 v41, v41
	v_rcp_f32_e32 v43, v43
	v_med3_f32 v46, v53, s49, v254
	v_med3_f32 v47, v54, s49, v254
	v_fmac_f32_e32 v55, v40, v61
	v_cvt_pk_fp8_f32 v46, v46, v47
	v_med3_f32 v47, v57, s49, v254
	v_med3_f32 v61, v58, s49, v254
	v_and_b32_e32 v56, 0xffff0000, v77
	v_and_b32_e32 v62, 0xffff0000, v73
	v_cvt_pk_fp8_f32 v47, v47, v61
	v_mul_f32_e32 v32, v32, v52
	v_lshlrev_b32_e32 v59, 16, v79
	v_and_b32_e32 v60, 0xffff0000, v79
	v_lshlrev_b32_e32 v73, 16, v75
	v_and_b32_e32 v74, 0xffff0000, v75
	v_fmac_f32_e32 v56, v42, v62
	v_mul_f32_e32 v32, 0xbfb8aa3b, v32
	v_fmac_f32_e32 v59, v41, v73
	v_fmac_f32_e32 v60, v43, v74
	v_med3_f32 v50, v55, s49, v254
	v_med3_f32 v51, v56, s49, v254
	v_exp_f32_e32 v32, v32
	v_cvt_pk_fp8_f32 v46, v50, v51 op_sel:[0,0,1]
	v_med3_f32 v50, v59, s49, v254
	v_med3_f32 v51, v60, s49, v254
	v_lshl_add_u64 v[48:49], v[92:93], 0, v[152:153]
	v_cvt_pk_fp8_f32 v47, v50, v51 op_sel:[0,0,1]
	v_lshl_add_u64 v[44:45], v[48:49], 0, s[6:7]
	v_mul_f32_e32 v33, v33, v52
	v_cvt_pk_bf16_f32 v40, v53, v54
	v_cvt_pk_bf16_f32 v41, v55, v56
	v_lshl_add_u64 v[50:51], v[44:45], 1, s[10:11]
	v_add_f32_e32 v32, 1.0, v32
	v_mul_f32_e32 v33, 0xbfb8aa3b, v33
	v_cvt_pk_bf16_f32 v42, v57, v58
	v_cvt_pk_bf16_f32 v43, v59, v60
	global_store_dwordx4 v[50:51], v[40:43], off
	v_rcp_f32_e32 v32, v32
	v_exp_f32_e32 v33, v33
	v_lshl_add_u64 v[40:41], s[18:19], 0, v[44:45]
	global_store_dwordx2 v[40:41], v[46:47], off
	v_mul_f32_e32 v40, v54, v54
	v_mul_f32_e32 v41, v56, v56
	v_fmac_f32_e32 v40, v53, v53
	v_fmac_f32_e32 v41, v55, v55
	v_add_f32_e32 v40, v40, v41
	v_mul_f32_e32 v41, v58, v58
	s_nop 0
	v_lshlrev_b32_e32 v45, 16, v70
	s_nop 0
	v_lshlrev_b32_e32 v58, 16, v66
	v_fmac_f32_e32 v45, v32, v58
	v_add_f32_e32 v32, 1.0, v33
	v_mul_f32_e32 v33, v38, v52
	v_mul_f32_e32 v34, v34, v52
	v_mul_f32_e32 v33, 0xbfb8aa3b, v33
	v_mul_f32_e32 v34, 0xbfb8aa3b, v34
	v_rcp_f32_e32 v32, v32
	v_exp_f32_e32 v33, v33
	v_exp_f32_e32 v34, v34
	v_mul_f32_e32 v42, v60, v60
	v_fmac_f32_e32 v42, v59, v59
	v_and_b32_e32 v46, 0xffff0000, v70
	v_and_b32_e32 v59, 0xffff0000, v66
	v_mul_f32_e32 v36, v36, v52
	v_mul_f32_e32 v37, v37, v52
	v_fmac_f32_e32 v46, v32, v59
	v_add_f32_e32 v32, 1.0, v33
	v_add_f32_e32 v33, 1.0, v34
	v_mul_f32_e32 v34, v39, v52
	v_mul_f32_e32 v36, 0xbfb8aa3b, v36
	v_mul_f32_e32 v37, 0xbfb8aa3b, v37
	v_mul_f32_e32 v34, 0xbfb8aa3b, v34
	v_mul_f32_e32 v35, v35, v52
	v_exp_f32_e32 v36, v36
	v_exp_f32_e32 v37, v37
	v_exp_f32_e32 v34, v34
	v_mul_f32_e32 v35, 0xbfb8aa3b, v35
	v_exp_f32_e32 v35, v35
	v_add_f32_e32 v36, 1.0, v36
	v_add_f32_e32 v37, 1.0, v37
	v_add_f32_e32 v34, 1.0, v34
	v_rcp_f32_e32 v36, v36
	v_rcp_f32_e32 v37, v37
	v_rcp_f32_e32 v32, v32
	v_rcp_f32_e32 v33, v33
	v_rcp_f32_e32 v34, v34
	v_add_f32_e32 v35, 1.0, v35
	v_fmac_f32_e32 v41, v57, v57
	v_rcp_f32_e32 v35, v35
	v_add_f32_e32 v41, v41, v42
	v_add_f32_e32 v40, v40, v41
	v_lshlrev_b32_e32 v41, 16, v68
	v_and_b32_e32 v42, 0xffff0000, v68
	v_lshlrev_b32_e32 v43, 16, v69
	v_and_b32_e32 v44, 0xffff0000, v69
	v_lshlrev_b32_e32 v47, 16, v71
	v_lshlrev_b32_e32 v54, 16, v64
	v_and_b32_e32 v55, 0xffff0000, v64
	v_lshlrev_b32_e32 v56, 16, v65
	v_and_b32_e32 v57, 0xffff0000, v65
	v_lshlrev_b32_e32 v60, 16, v67
	v_and_b32_e32 v53, 0xffff0000, v71
	v_and_b32_e32 v61, 0xffff0000, v67
	v_fmac_f32_e32 v41, v36, v54
	v_fmac_f32_e32 v42, v37, v55
	v_fmac_f32_e32 v43, v32, v56
	v_fmac_f32_e32 v47, v33, v60
	v_fmac_f32_e32 v44, v34, v57
	v_cvt_pk_bf16_f32 v32, v41, v42
	v_cvt_pk_bf16_f32 v33, v43, v44
	v_fmac_f32_e32 v53, v35, v61
	v_cvt_pk_bf16_f32 v34, v45, v46
	v_cvt_pk_bf16_f32 v35, v47, v53
	global_store_dwordx4 v[50:51], v[32:35], off offset:256
	v_med3_f32 v36, v46, s49, v254
	s_add_u32 s28, s18, s95
	v_med3_f32 v32, v41, s49, v254
	v_med3_f32 v33, v42, s49, v254
	v_cvt_pk_fp8_f32 v32, v32, v33
	v_med3_f32 v33, v45, s49, v254
	v_cvt_pk_fp8_f32 v33, v33, v36
	v_med3_f32 v34, v43, s49, v254
	v_med3_f32 v35, v44, s49, v254
	v_cvt_pk_fp8_f32 v32, v34, v35 op_sel:[0,0,1]
	v_med3_f32 v34, v47, s49, v254
	v_med3_f32 v35, v53, s49, v254
	v_cvt_pk_fp8_f32 v33, v34, v35 op_sel:[0,0,1]
	v_mul_f32_e32 v34, v42, v42
	v_mul_f32_e32 v35, v44, v44
	v_fmac_f32_e32 v34, v41, v41
	v_fmac_f32_e32 v35, v43, v43
	v_add_f32_e32 v34, v34, v35
	v_mul_f32_e32 v35, v46, v46
	v_mul_f32_e32 v36, v53, v53
	v_fmac_f32_e32 v35, v45, v45
	v_fmac_f32_e32 v36, v47, v47
	v_add_f32_e32 v35, v35, v36
	v_add_f32_e32 v34, v34, v35
	v_add_f32_e32 v36, v40, v34
	ds_swizzle_b32 v37, v36 offset:swizzle(SWAP,16)
	s_addc_u32 s29, s19, s96
	v_lshl_add_u64 v[34:35], s[28:29], 0, v[48:49]
	global_store_dwordx2 v[34:35], v[32:33], off
	s_waitcnt lgkmcnt(0)
	v_add_f32_e32 v32, v36, v37
	v_mov_b32_e32 v33, v32
	s_nop 1
	v_permlane32_swap_b32_e32 v32, v33
	s_and_saveexec_b64 s[28:29], vcc
	s_cbranch_execz .LBB0_1959
	s_lshl_b32 s54, s31, 2
	v_add_f32_e32 v34, v32, v33
	s_ashr_i32 s55, s54, 31
	v_lshl_add_u64 v[32:33], s[12:13], 0, v[88:89]
	v_lshl_add_u64 v[32:33], s[54:55], 2, v[32:33]
	s_lshl_b32 s54, s59, 2
	s_mov_b32 s55, s40
	v_lshl_add_u64 v[32:33], v[32:33], 0, s[54:55]
	global_store_dword v[32:33], v34, off
; template <int MASK> __device__ __forceinline__ float swz_f(float v) { return __builtin_bit_cast(float, __builtin_amdgcn_ds_swizzle(__builtin_bit_cast(int, v), (MASK << 10) | 0x1f)); }
; __device__ __forceinline__ float rstd_q(const float* ssq, int row, int fq) {
;     const f32x4 p = *(const f32x4*)(ssq + 16 * (size_t)row + 4 * fq); float s = (p.x + p.y) + (p.z + p.w); s += swz_f<16>(s); s = sum_x32(s);
;     return __builtin_amdgcn_rsqf(s * (1.f / 1024.f) + EPS);
;     __device__ __forceinline__ void operator()(const f32x4 (&acc)[2][2][4][2], const Unit& u, int wr, int wc, int fr, int fq) const {
;     ...
;             u32x4 hv[4][2], pv[4][2]; float rs4[4];
; #pragma unroll
;             for (int m = mb; m < mb + MBAT; ++m) { const int row = EPI_ROWS(ai, m); rs4[m] = 0.f; if (MODE == 1) rs4[m] = rstd_q(ssq_in, row, fq) * ascale;
; #pragma unroll
;                 for (int bj = 0; bj < 2; ++bj) { const size_t off = (size_t)row * DM + u.pn * BM + bj * HALF + wc * 32 + 8 * fq; hv[m][bj] = *(const u32x4*)(hin + off); if (MODE == 1) pv[m][bj] = *(const u32x4*)(PP + off); } }
; #pragma unroll
;             for (int m = mb; m < mb + MBAT; ++m) { const int row = EPI_ROWS(ai, m); const float rs = rs4[m]; float ss = 0.f;
; #pragma unroll
;                 for (int bj = 0; bj < 2; ++bj) { const size_t off = (size_t)row * DM + u.pn * BM + bj * HALF + wc * 32 + 8 * fq;
;                     f32x4 v0, v1; unpack8(hv[m][bj], v0, v1); const f32x4 a0 = acc[ai][bj][m][0], a1 = acc[ai][bj][m][1];
;                     if (MODE == 0) { v0 = v0 + a0 * ascale; v1 = v1 + a1 * ascale; }
;                     else { f32x4 p0, p1; unpack8(pv[m][bj], p0, p1);
; #pragma unroll
;                         for (int e = 0; e < 4; ++e) { v0[e] += fast_sigmoid(a0[e] * rs) * p0[e]; v1[e] += fast_sigmoid(a1[e] * rs) * p1[e]; } }
;                     if (outf) { *(f32x4*)(outf + off) = v0; *(f32x4*)(outf + off + 4) = v1; }
;                     else *(u32x4*)(hout + off) = pack8(v0, v1);
;                     if (h8) { u32x2 w8; w8.x = pk4_fp8(v0[0], v0[1], v0[2], v0[3]); w8.y = pk4_fp8(v1[0], v1[1], v1[2], v1[3]); *(u32x2*)(h8 + off) = w8; }
;                     ss += ((v0[0] * v0[0] + v0[1] * v0[1]) + (v0[2] * v0[2] + v0[3] * v0[3])) + ((v1[0] * v1[0] + v1[1] * v1[1]) + (v1[2] * v1[2] + v1[3] * v1[3])); }
.LBB0_1959:
	s_or_b64 exec, exec, s[28:29]
	v_add_u32_e32 v36, 0xa0, v158
	v_ashrrev_i32_e32 v37, 31, v36
	v_lshlrev_b64 v[58:59], 6, v[36:37]
	v_lshl_add_u64 v[32:33], v[156:157], 0, v[58:59]
	s_nop 0
	v_lshlrev_b64 v[62:63], 10, v[36:37]
	v_add_u32_e32 v36, 0xb0, v158
	v_ashrrev_i32_e32 v37, 31, v36
	v_lshlrev_b64 v[56:57], 6, v[36:37]
	v_lshlrev_b64 v[60:61], 10, v[36:37]
	s_add_u32 s28, s18, s95
	s_addc_u32 s29, s19, s96
	s_waitcnt vmcnt(8)
	v_mov_b32_e32 v32, v200
	v_mov_b32_e32 v33, v201
	v_mov_b32_e32 v34, v202
	v_mov_b32_e32 v35, v203
	v_add_f32_e32 v32, v32, v33
	v_add_f32_e32 v33, v34, v35
	v_add_f32_e32 v32, v32, v33
	ds_swizzle_b32 v33, v32 offset:swizzle(SWAP,16)
	s_waitcnt lgkmcnt(0)
	v_add_f32_e32 v32, v32, v33
	v_mov_b32_e32 v33, v32
	s_nop 1
	v_permlane32_swap_b32_e32 v32, v33
	v_add_f32_e32 v32, v32, v33
	v_fmamk_f32 v32, v32, 0x3a800000, v230
	v_rsq_f32_e32 v66, v32
	v_lshl_add_u64 v[32:33], v[62:63], 0, v[154:155]
	v_lshlrev_b64 v[32:33], 1, v[32:33]
	v_lshl_add_u64 v[34:35], s[2:3], 0, v[32:33]
	v_mov_b32_e32 v68, v204
	v_mov_b32_e32 v69, v205
	v_mov_b32_e32 v70, v206
	v_mov_b32_e32 v71, v207
	v_lshl_add_u64 v[32:33], s[14:15], 0, v[32:33]
	v_mov_b32_e32 v72, v208
	v_mov_b32_e32 v73, v209
	v_mov_b32_e32 v74, v210
	v_mov_b32_e32 v75, v211
	v_mov_b32_e32 v52, v212
	v_mov_b32_e32 v53, v213
	v_mov_b32_e32 v54, v214
	v_mov_b32_e32 v55, v215
	v_mov_b32_e32 v48, v216
	v_mov_b32_e32 v49, v217
	v_mov_b32_e32 v50, v218
	v_mov_b32_e32 v51, v219
	v_lshl_add_u64 v[32:33], v[156:157], 0, v[56:57]
	v_mov_b32_e32 v32, v220
	v_mov_b32_e32 v33, v221
	v_mov_b32_e32 v34, v222
	v_mov_b32_e32 v35, v223
	v_mul_f32_e32 v24, v24, v66
	v_mul_f32_e32 v24, 0xbfb8aa3b, v24
	v_exp_f32_e32 v24, v24
	v_mul_f32_e32 v28, v28, v66
	v_mul_f32_e32 v28, 0xbfb8aa3b, v28
	v_exp_f32_e32 v28, v28
	v_add_f32_e32 v24, 1.0, v24
	v_rcp_f32_e32 v24, v24
	v_lshl_add_u64 v[62:63], v[62:63], 0, v[152:153]
	v_add_f32_e32 v28, 1.0, v28
	v_rcp_f32_e32 v28, v28
	v_mul_f32_e32 v16, v16, v66
	v_mul_f32_e32 v16, 0xbfb8aa3b, v16
	v_exp_f32_e32 v16, v16
	v_mul_f32_e32 v20, v20, v66
	v_mul_f32_e32 v20, 0xbfb8aa3b, v20
	v_exp_f32_e32 v20, v20
	v_add_f32_e32 v16, 1.0, v16
	v_rcp_f32_e32 v16, v16
	v_add_f32_e32 v20, 1.0, v20
	v_rcp_f32_e32 v20, v20
	s_nop 0
	v_lshlrev_b32_e32 v81, 16, v74
	v_lshlrev_b32_e32 v77, 16, v70
	v_fmac_f32_e32 v77, v24, v81
	v_mul_f32_e32 v24, v29, v66
	v_mul_f32_e32 v24, 0xbfb8aa3b, v24
	v_exp_f32_e32 v24, v24
	v_lshlrev_b32_e32 v67, 16, v68
	v_and_b32_e32 v68, 0xffff0000, v68
	v_lshlrev_b32_e32 v79, 16, v72
	v_add_f32_e32 v24, 1.0, v24
	v_rcp_f32_e32 v24, v24
	v_and_b32_e32 v72, 0xffff0000, v72
	v_and_b32_e32 v70, 0xffff0000, v70
	v_and_b32_e32 v74, 0xffff0000, v74
	v_fmac_f32_e32 v68, v24, v72
	v_mul_f32_e32 v24, v25, v66
	v_mul_f32_e32 v24, 0xbfb8aa3b, v24
	v_exp_f32_e32 v24, v24
	v_lshlrev_b32_e32 v76, 16, v69
	v_lshlrev_b32_e32 v80, 16, v73
	v_lshlrev_b32_e32 v78, 16, v71
	v_add_f32_e32 v24, 1.0, v24
	v_rcp_f32_e32 v24, v24
	v_lshlrev_b32_e32 v82, 16, v75
	v_and_b32_e32 v69, 0xffff0000, v69
	v_and_b32_e32 v73, 0xffff0000, v73
	v_fmac_f32_e32 v70, v24, v74
	v_mul_f32_e32 v24, v30, v66
	v_mul_f32_e32 v24, 0xbfb8aa3b, v24
	v_exp_f32_e32 v24, v24
	s_nop 0
	v_add_f32_e32 v32, v32, v33
	v_add_f32_e32 v33, v34, v35
	v_add_f32_e32 v32, v32, v33
	v_add_f32_e32 v24, 1.0, v24
	v_rcp_f32_e32 v24, v24
	ds_swizzle_b32 v33, v32 offset:swizzle(SWAP,16)
	v_and_b32_e32 v71, 0xffff0000, v71
	v_and_b32_e32 v75, 0xffff0000, v75
	v_fmac_f32_e32 v76, v24, v80
	v_mul_f32_e32 v24, v26, v66
	v_mul_f32_e32 v24, 0xbfb8aa3b, v24
	v_exp_f32_e32 v24, v24
	s_waitcnt lgkmcnt(0)
	v_add_f32_e32 v64, v32, v33
	v_lshl_add_u64 v[32:33], v[60:61], 0, v[154:155]
	v_lshlrev_b64 v[32:33], 1, v[32:33]
	v_add_f32_e32 v24, 1.0, v24
	v_rcp_f32_e32 v24, v24
	v_lshl_add_u64 v[34:35], s[2:3], 0, v[32:33]
	v_lshl_add_u64 v[32:33], s[14:15], 0, v[32:33]
	v_mov_b32_e32 v44, v236
	v_mov_b32_e32 v45, v237
	v_mov_b32_e32 v46, v238
	v_mov_b32_e32 v47, v239
	v_fmac_f32_e32 v78, v24, v82
	v_mul_f32_e32 v24, v31, v66
	v_mul_f32_e32 v24, 0xbfb8aa3b, v24
	v_exp_f32_e32 v24, v24
	v_lshl_add_u64 v[30:31], v[62:63], 0, s[6:7]
	v_mov_b32_e32 v40, v240
	v_mov_b32_e32 v41, v241
	v_mov_b32_e32 v42, v242
	v_mov_b32_e32 v43, v243
	v_mov_b32_e32 v36, v244
	v_mov_b32_e32 v37, v245
	v_mov_b32_e32 v38, v246
	v_mov_b32_e32 v39, v247
	s_nop 0
	v_mov_b32_e32 v32, v248
	v_mov_b32_e32 v33, v249
	v_mov_b32_e32 v34, v250
	v_mov_b32_e32 v35, v251
	v_fmac_f32_e32 v67, v28, v79
	v_add_f32_e32 v24, 1.0, v24
	v_rcp_f32_e32 v24, v24
	v_cvt_pk_bf16_f32 v26, v67, v68
	v_mov_b32_e32 v65, v64
	s_nop 1
	v_permlane32_swap_b32_e32 v64, v65
	v_fmac_f32_e32 v69, v24, v73
	v_mul_f32_e32 v24, v27, v66
	v_mul_f32_e32 v24, 0xbfb8aa3b, v24
	v_exp_f32_e32 v24, v24
	v_cvt_pk_bf16_f32 v27, v76, v69
	v_cvt_pk_bf16_f32 v28, v77, v70
	s_nop 0
	v_add_f32_e32 v24, 1.0, v24
	v_rcp_f32_e32 v24, v24
	s_nop 0
	v_fmac_f32_e32 v71, v24, v75
	v_lshl_add_u64 v[24:25], v[30:31], 1, s[10:11]
	v_cvt_pk_bf16_f32 v29, v78, v71
	global_store_dwordx4 v[24:25], v[26:29], off
	v_med3_f32 v72, v71, s49, v254
	s_nop 0
	v_med3_f32 v26, v67, s49, v254
	v_med3_f32 v27, v68, s49, v254
	v_cvt_pk_fp8_f32 v26, v26, v27
	v_med3_f32 v28, v76, s49, v254
	v_med3_f32 v29, v69, s49, v254
	v_med3_f32 v27, v77, s49, v254
	v_cvt_pk_fp8_f32 v26, v28, v29 op_sel:[0,0,1]
	v_med3_f32 v28, v70, s49, v254
	v_cvt_pk_fp8_f32 v27, v27, v28
	v_med3_f32 v29, v78, s49, v254
	v_cvt_pk_fp8_f32 v27, v29, v72 op_sel:[0,0,1]
	v_lshl_add_u64 v[28:29], s[18:19], 0, v[30:31]
	v_lshlrev_b32_e32 v31, 16, v54
	v_and_b32_e32 v30, 0xffff0000, v53
	global_store_dwordx2 v[28:29], v[26:27], off
	v_mul_f32_e32 v26, v68, v68
; template <int MASK> __device__ __forceinline__ float swz_f(float v) { return __builtin_bit_cast(float, __builtin_amdgcn_ds_swizzle(__builtin_bit_cast(int, v), (MASK << 10) | 0x1f)); }
; __device__ __forceinline__ float sum_x32(float v) { const unsigned u = __builtin_bit_cast(unsigned, v); auto rr = __builtin_amdgcn_permlane32_swap(u, u, false, false); return __builtin_bit_cast(float, (unsigned)rr[0]) + __builtin_bit_cast(float, (unsigned)rr[1]); }
; __device__ __forceinline__ float fast_sigmoid(float x) { return __builtin_amdgcn_rcpf(1.f + __builtin_amdgcn_exp2f(-LOG2E * x)); }
; __device__ __forceinline__ u32x4 pack8(const f32x4 a, const f32x4 b) { u32x4 w; w.x = cvt_pk_bf16(a[0], a[1]); w.y = cvt_pk_bf16(a[2], a[3]); w.z = cvt_pk_bf16(b[0], b[1]); w.w = cvt_pk_bf16(b[2], b[3]); return w; }
;     __device__ __forceinline__ void operator()(const f32x4 (&acc)[2][2][4][2], const Unit& u, int wr, int wc, int fr, int fq) const {
;     ...
;             for (int m = mb; m < mb + MBAT; ++m) { const int row = EPI_ROWS(ai, m); const float rs = rs4[m]; float ss = 0.f;
; #pragma unroll
;                 for (int bj = 0; bj < 2; ++bj) { const size_t off = (size_t)row * DM + u.pn * BM + bj * HALF + wc * 32 + 8 * fq;
;                     f32x4 v0, v1; unpack8(hv[m][bj], v0, v1); const f32x4 a0 = acc[ai][bj][m][0], a1 = acc[ai][bj][m][1];
;                     if (MODE == 0) { v0 = v0 + a0 * ascale; v1 = v1 + a1 * ascale; }
;                     else { f32x4 p0, p1; unpack8(pv[m][bj], p0, p1);
; #pragma unroll
;                         for (int e = 0; e < 4; ++e) { v0[e] += fast_sigmoid(a0[e] * rs) * p0[e]; v1[e] += fast_sigmoid(a1[e] * rs) * p1[e]; } }
;                     if (outf) { *(f32x4*)(outf + off) = v0; *(f32x4*)(outf + off + 4) = v1; }
;                     else *(u32x4*)(hout + off) = pack8(v0, v1);
;                     if (h8) { u32x2 w8; w8.x = pk4_fp8(v0[0], v0[1], v0[2], v0[3]); w8.y = pk4_fp8(v1[0], v1[1], v1[2], v1[3]); *(u32x2*)(h8 + off) = w8; }
;                     ss += ((v0[0] * v0[0] + v0[1] * v0[1]) + (v0[2] * v0[2] + v0[3] * v0[3])) + ((v1[0] * v1[0] + v1[1] * v1[1]) + (v1[2] * v1[2] + v1[3] * v1[3])); }
;                 ss += swz_f<16>(ss); ss = sum_x32(ss);
;                 if (fq == 0) ssq_out[(size_t)row * 16 + u.pn * 4 + wc] = ss; }
	v_lshlrev_b32_e32 v68, 16, v50
	v_fmac_f32_e32 v31, v16, v68
	v_mul_f32_e32 v16, v21, v66
	v_mul_f32_e32 v16, 0xbfb8aa3b, v16
	v_exp_f32_e32 v16, v16
	v_mul_f32_e32 v27, v69, v69
	v_fmac_f32_e32 v26, v67, v67
	v_fmac_f32_e32 v27, v76, v76
	v_add_f32_e32 v16, 1.0, v16
	v_add_f32_e32 v26, v26, v27
	v_mul_f32_e32 v27, v70, v70
	v_mul_f32_e32 v28, v71, v71
	v_rcp_f32_e32 v16, v16
	v_fmac_f32_e32 v27, v77, v77
	v_fmac_f32_e32 v28, v78, v78
	v_add_f32_e32 v27, v27, v28
	v_add_f32_e32 v26, v26, v27
	v_lshlrev_b32_e32 v27, 16, v52
	v_and_b32_e32 v28, 0xffff0000, v52
	v_lshlrev_b32_e32 v29, 16, v53
	v_and_b32_e32 v52, 0xffff0000, v54
	v_lshlrev_b32_e32 v53, 16, v55
	v_and_b32_e32 v54, 0xffff0000, v55
	v_lshlrev_b32_e32 v55, 16, v48
	v_and_b32_e32 v48, 0xffff0000, v48
	v_fmac_f32_e32 v28, v16, v48
	v_mul_f32_e32 v16, v17, v66
	v_mul_f32_e32 v16, 0xbfb8aa3b, v16
	v_exp_f32_e32 v16, v16
	v_and_b32_e32 v50, 0xffff0000, v50
	v_lshlrev_b32_e32 v67, 16, v49
	v_lshlrev_b32_e32 v69, 16, v51
	v_add_f32_e32 v16, 1.0, v16
	v_rcp_f32_e32 v16, v16
	v_and_b32_e32 v49, 0xffff0000, v49
	v_and_b32_e32 v51, 0xffff0000, v51
	v_fmac_f32_e32 v27, v20, v55
	v_fmac_f32_e32 v52, v16, v50
	v_mul_f32_e32 v16, v22, v66
	v_mul_f32_e32 v16, 0xbfb8aa3b, v16
	v_exp_f32_e32 v16, v16
	s_nop 0
	v_add_f32_e32 v16, 1.0, v16
	v_rcp_f32_e32 v16, v16
	s_nop 0
	v_fmac_f32_e32 v29, v16, v67
	v_mul_f32_e32 v16, v18, v66
	v_mul_f32_e32 v16, 0xbfb8aa3b, v16
	v_exp_f32_e32 v16, v16
	s_nop 0
	v_add_f32_e32 v16, 1.0, v16
	v_rcp_f32_e32 v16, v16
	s_nop 0
	v_fmac_f32_e32 v53, v16, v69
	v_mul_f32_e32 v16, v23, v66
	v_mul_f32_e32 v16, 0xbfb8aa3b, v16
	v_exp_f32_e32 v16, v16
	s_nop 0
	v_add_f32_e32 v16, 1.0, v16
	v_rcp_f32_e32 v16, v16
	s_nop 0
	v_fmac_f32_e32 v30, v16, v49
	v_mul_f32_e32 v16, v19, v66
	v_mul_f32_e32 v16, 0xbfb8aa3b, v16
	v_exp_f32_e32 v16, v16
	s_nop 0
	v_add_f32_e32 v16, 1.0, v16
	v_rcp_f32_e32 v16, v16
	s_nop 0
	v_fmac_f32_e32 v54, v16, v51
	v_cvt_pk_bf16_f32 v16, v27, v28
	v_cvt_pk_bf16_f32 v17, v29, v30
	v_cvt_pk_bf16_f32 v18, v31, v52
	v_cvt_pk_bf16_f32 v19, v53, v54
	global_store_dwordx4 v[24:25], v[16:19], off offset:256
	v_med3_f32 v20, v54, s49, v254
	s_nop 0
	v_med3_f32 v16, v27, s49, v254
	v_med3_f32 v17, v28, s49, v254
	v_cvt_pk_fp8_f32 v16, v16, v17
	v_med3_f32 v18, v29, s49, v254
	v_med3_f32 v19, v30, s49, v254
	v_med3_f32 v17, v31, s49, v254
	v_cvt_pk_fp8_f32 v16, v18, v19 op_sel:[0,0,1]
	v_med3_f32 v18, v52, s49, v254
	v_cvt_pk_fp8_f32 v17, v17, v18
	v_med3_f32 v19, v53, s49, v254
	v_cvt_pk_fp8_f32 v17, v19, v20 op_sel:[0,0,1]
	v_lshl_add_u64 v[18:19], s[28:29], 0, v[62:63]
	global_store_dwordx2 v[18:19], v[16:17], off
	v_mul_f32_e32 v16, v28, v28
	v_mul_f32_e32 v17, v30, v30
	v_fmac_f32_e32 v16, v27, v27
	v_fmac_f32_e32 v17, v29, v29
	v_add_f32_e32 v16, v16, v17
	v_mul_f32_e32 v17, v52, v52
	v_mul_f32_e32 v18, v54, v54
	v_fmac_f32_e32 v17, v31, v31
	v_fmac_f32_e32 v18, v53, v53
	v_add_f32_e32 v17, v17, v18
	v_add_f32_e32 v16, v16, v17
	v_add_f32_e32 v16, v26, v16
	ds_swizzle_b32 v17, v16 offset:swizzle(SWAP,16)
	s_waitcnt lgkmcnt(0)
	v_add_f32_e32 v16, v16, v17
	v_mov_b32_e32 v17, v16
	s_nop 1
	v_permlane32_swap_b32_e32 v16, v17
	s_and_saveexec_b64 s[28:29], vcc
	s_cbranch_execz .LBB0_1961
	s_lshl_b32 s54, s31, 2
	v_add_f32_e32 v18, v16, v17
	s_ashr_i32 s55, s54, 31
	v_lshl_add_u64 v[16:17], s[12:13], 0, v[58:59]
	v_lshl_add_u64 v[16:17], s[54:55], 2, v[16:17]
	s_lshl_b32 s54, s59, 2
	s_mov_b32 s55, s40
	v_lshl_add_u64 v[16:17], v[16:17], 0, s[54:55]
	global_store_dword v[16:17], v18, off
; template <int MASK> __device__ __forceinline__ float swz_f(float v) { return __builtin_bit_cast(float, __builtin_amdgcn_ds_swizzle(__builtin_bit_cast(int, v), (MASK << 10) | 0x1f)); }
; __device__ __forceinline__ float sum_x32(float v) { const unsigned u = __builtin_bit_cast(unsigned, v); auto rr = __builtin_amdgcn_permlane32_swap(u, u, false, false); return __builtin_bit_cast(float, (unsigned)rr[0]) + __builtin_bit_cast(float, (unsigned)rr[1]); }
; __device__ __forceinline__ float fast_sigmoid(float x) { return __builtin_amdgcn_rcpf(1.f + __builtin_amdgcn_exp2f(-LOG2E * x)); }
; __device__ __forceinline__ float rstd_q(const float* ssq, int row, int fq) {
;     const f32x4 p = *(const f32x4*)(ssq + 16 * (size_t)row + 4 * fq); float s = (p.x + p.y) + (p.z + p.w); s += swz_f<16>(s); s = sum_x32(s);
;     return __builtin_amdgcn_rsqf(s * (1.f / 1024.f) + EPS);
;     __device__ __forceinline__ void operator()(const f32x4 (&acc)[2][2][4][2], const Unit& u, int wr, int wc, int fr, int fq) const {
;     ...
;             for (int m = mb; m < mb + MBAT; ++m) { const int row = EPI_ROWS(ai, m); const float rs = rs4[m]; float ss = 0.f;
; #pragma unroll
;                 for (int bj = 0; bj < 2; ++bj) { const size_t off = (size_t)row * DM + u.pn * BM + bj * HALF + wc * 32 + 8 * fq;
;                     f32x4 v0, v1; unpack8(hv[m][bj], v0, v1); const f32x4 a0 = acc[ai][bj][m][0], a1 = acc[ai][bj][m][1];
;                     if (MODE == 0) { v0 = v0 + a0 * ascale; v1 = v1 + a1 * ascale; }
;                     else { f32x4 p0, p1; unpack8(pv[m][bj], p0, p1);
; #pragma unroll
;                         for (int e = 0; e < 4; ++e) { v0[e] += fast_sigmoid(a0[e] * rs) * p0[e]; v1[e] += fast_sigmoid(a1[e] * rs) * p1[e]; } }
;                     if (outf) { *(f32x4*)(outf + off) = v0; *(f32x4*)(outf + off + 4) = v1; }
;                     else *(u32x4*)(hout + off) = pack8(v0, v1);
;                     if (h8) { u32x2 w8; w8.x = pk4_fp8(v0[0], v0[1], v0[2], v0[3]); w8.y = pk4_fp8(v1[0], v1[1], v1[2], v1[3]); *(u32x2*)(h8 + off) = w8; }
;                     ss += ((v0[0] * v0[0] + v0[1] * v0[1]) + (v0[2] * v0[2] + v0[3] * v0[3])) + ((v1[0] * v1[0] + v1[1] * v1[1]) + (v1[2] * v1[2] + v1[3] * v1[3])); }
;                 ss += swz_f<16>(ss); ss = sum_x32(ss);
;                 if (fq == 0) ssq_out[(size_t)row * 16 + u.pn * 4 + wc] = ss; }
.LBB0_1961:
	s_or_b64 exec, exec, s[28:29]
	v_add_f32_e32 v16, v64, v65
	v_fmamk_f32 v16, v16, 0x3a800000, v230
	v_rsq_f32_e32 v20, v16
	s_nop 0
	v_lshlrev_b32_e32 v25, 16, v46
	s_nop 0
	v_lshlrev_b32_e32 v31, 16, v42
	v_and_b32_e32 v26, 0xffff0000, v46
	v_mul_f32_e32 v8, v8, v20
	v_mul_f32_e32 v8, 0xbfb8aa3b, v8
	v_exp_f32_e32 v8, v8
	v_mul_f32_e32 v9, v9, v20
	v_mul_f32_e32 v9, 0xbfb8aa3b, v9
	v_exp_f32_e32 v9, v9
	v_add_f32_e32 v8, 1.0, v8
	v_rcp_f32_e32 v8, v8
	v_mul_f32_e32 v10, v10, v20
	v_mul_f32_e32 v10, 0xbfb8aa3b, v10
	v_mul_f32_e32 v12, v12, v20
	v_fmac_f32_e32 v25, v8, v31
	v_add_f32_e32 v8, 1.0, v9
	v_mul_f32_e32 v9, v14, v20
	v_mul_f32_e32 v9, 0xbfb8aa3b, v9
	v_mul_f32_e32 v13, v13, v20
	v_rcp_f32_e32 v8, v8
	v_exp_f32_e32 v9, v9
	v_exp_f32_e32 v10, v10
	v_mul_f32_e32 v12, 0xbfb8aa3b, v12
	v_mul_f32_e32 v13, 0xbfb8aa3b, v13
	v_exp_f32_e32 v12, v12
	v_exp_f32_e32 v13, v13
	v_lshlrev_b32_e32 v18, 16, v40
	v_and_b32_e32 v19, 0xffff0000, v40
	v_and_b32_e32 v40, 0xffff0000, v42
	v_fmac_f32_e32 v26, v8, v40
	v_add_f32_e32 v8, 1.0, v9
	v_add_f32_e32 v9, 1.0, v10
	v_mul_f32_e32 v10, v15, v20
	v_mul_f32_e32 v10, 0xbfb8aa3b, v10
	v_mul_f32_e32 v11, v11, v20
	v_add_f32_e32 v12, 1.0, v12
	v_add_f32_e32 v13, 1.0, v13
	v_exp_f32_e32 v10, v10
	v_mul_f32_e32 v11, 0xbfb8aa3b, v11
	v_rcp_f32_e32 v12, v12
	v_rcp_f32_e32 v13, v13
	v_exp_f32_e32 v11, v11
	v_rcp_f32_e32 v8, v8
	v_lshlrev_b32_e32 v21, 16, v44
	v_and_b32_e32 v22, 0xffff0000, v44
	v_add_f32_e32 v10, 1.0, v10
	v_fmac_f32_e32 v21, v12, v18
	v_fmac_f32_e32 v22, v13, v19
	v_rcp_f32_e32 v10, v10
	v_add_f32_e32 v11, 1.0, v11
	v_lshlrev_b32_e32 v23, 16, v45
	v_lshlrev_b32_e32 v29, 16, v41
	v_rcp_f32_e32 v9, v9
	v_rcp_f32_e32 v11, v11
	v_med3_f32 v14, v21, s49, v254
	v_med3_f32 v15, v22, s49, v254
	v_fmac_f32_e32 v23, v8, v29
	v_cvt_pk_fp8_f32 v14, v14, v15
	v_med3_f32 v15, v25, s49, v254
	v_med3_f32 v29, v26, s49, v254
	v_and_b32_e32 v24, 0xffff0000, v45
	v_and_b32_e32 v30, 0xffff0000, v41
	v_cvt_pk_fp8_f32 v15, v15, v29
	v_mul_f32_e32 v0, v0, v20
	v_lshlrev_b32_e32 v27, 16, v47
	v_and_b32_e32 v28, 0xffff0000, v47
	v_lshlrev_b32_e32 v41, 16, v43
	v_and_b32_e32 v42, 0xffff0000, v43
	v_fmac_f32_e32 v24, v10, v30
	v_mul_f32_e32 v0, 0xbfb8aa3b, v0
	v_fmac_f32_e32 v27, v9, v41
	v_fmac_f32_e32 v28, v11, v42
	v_med3_f32 v18, v23, s49, v254
	v_med3_f32 v19, v24, s49, v254
	v_exp_f32_e32 v0, v0
	v_cvt_pk_fp8_f32 v14, v18, v19 op_sel:[0,0,1]
	v_med3_f32 v18, v27, s49, v254
	v_med3_f32 v19, v28, s49, v254
	v_lshl_add_u64 v[16:17], v[60:61], 0, v[152:153]
	v_cvt_pk_fp8_f32 v15, v18, v19 op_sel:[0,0,1]
	v_lshl_add_u64 v[12:13], v[16:17], 0, s[6:7]
	v_mul_f32_e32 v1, v1, v20
	v_cvt_pk_bf16_f32 v8, v21, v22
	v_cvt_pk_bf16_f32 v9, v23, v24
	v_lshl_add_u64 v[18:19], v[12:13], 1, s[10:11]
	v_add_f32_e32 v0, 1.0, v0
	v_mul_f32_e32 v1, 0xbfb8aa3b, v1
	v_cvt_pk_bf16_f32 v10, v25, v26
	v_cvt_pk_bf16_f32 v11, v27, v28
	global_store_dwordx4 v[18:19], v[8:11], off
	v_rcp_f32_e32 v0, v0
	v_exp_f32_e32 v1, v1
	v_lshl_add_u64 v[8:9], s[18:19], 0, v[12:13]
	global_store_dwordx2 v[8:9], v[14:15], off
	v_mul_f32_e32 v8, v22, v22
	v_mul_f32_e32 v9, v24, v24
	v_fmac_f32_e32 v8, v21, v21
	v_fmac_f32_e32 v9, v23, v23
	v_add_f32_e32 v8, v8, v9
	v_mul_f32_e32 v9, v26, v26
	s_nop 0
	v_lshlrev_b32_e32 v13, 16, v38
	s_nop 0
	v_lshlrev_b32_e32 v26, 16, v34
	v_fmac_f32_e32 v13, v0, v26
	v_add_f32_e32 v0, 1.0, v1
	v_mul_f32_e32 v1, v6, v20
	v_mul_f32_e32 v2, v2, v20
	v_mul_f32_e32 v1, 0xbfb8aa3b, v1
	v_mul_f32_e32 v2, 0xbfb8aa3b, v2
	v_rcp_f32_e32 v0, v0
	v_exp_f32_e32 v1, v1
	v_exp_f32_e32 v2, v2
	v_mul_f32_e32 v10, v28, v28
	v_fmac_f32_e32 v10, v27, v27
	v_and_b32_e32 v14, 0xffff0000, v38
	v_and_b32_e32 v27, 0xffff0000, v34
	v_mul_f32_e32 v4, v4, v20
	v_mul_f32_e32 v5, v5, v20
	v_fmac_f32_e32 v14, v0, v27
	v_add_f32_e32 v0, 1.0, v1
	v_add_f32_e32 v1, 1.0, v2
	v_mul_f32_e32 v2, v7, v20
	v_mul_f32_e32 v4, 0xbfb8aa3b, v4
	v_mul_f32_e32 v5, 0xbfb8aa3b, v5
	v_mul_f32_e32 v2, 0xbfb8aa3b, v2
	v_mul_f32_e32 v3, v3, v20
	v_exp_f32_e32 v4, v4
	v_exp_f32_e32 v5, v5
	v_exp_f32_e32 v2, v2
	v_mul_f32_e32 v3, 0xbfb8aa3b, v3
	v_exp_f32_e32 v3, v3
	v_add_f32_e32 v4, 1.0, v4
	v_add_f32_e32 v5, 1.0, v5
	v_add_f32_e32 v2, 1.0, v2
	v_rcp_f32_e32 v4, v4
	v_rcp_f32_e32 v5, v5
	v_rcp_f32_e32 v0, v0
	v_rcp_f32_e32 v1, v1
	v_rcp_f32_e32 v2, v2
	v_add_f32_e32 v3, 1.0, v3
	v_fmac_f32_e32 v9, v25, v25
	v_rcp_f32_e32 v3, v3
	v_add_f32_e32 v9, v9, v10
	v_add_f32_e32 v8, v8, v9
	v_lshlrev_b32_e32 v9, 16, v36
	v_and_b32_e32 v10, 0xffff0000, v36
	v_lshlrev_b32_e32 v11, 16, v37
	v_and_b32_e32 v12, 0xffff0000, v37
	v_lshlrev_b32_e32 v15, 16, v39
	v_lshlrev_b32_e32 v22, 16, v32
	v_and_b32_e32 v23, 0xffff0000, v32
	v_lshlrev_b32_e32 v24, 16, v33
	v_and_b32_e32 v25, 0xffff0000, v33
	v_lshlrev_b32_e32 v28, 16, v35
	v_and_b32_e32 v21, 0xffff0000, v39
	v_and_b32_e32 v29, 0xffff0000, v35
	v_fmac_f32_e32 v9, v4, v22
	v_fmac_f32_e32 v10, v5, v23
	v_fmac_f32_e32 v11, v0, v24
	v_fmac_f32_e32 v15, v1, v28
	v_fmac_f32_e32 v12, v2, v25
	v_cvt_pk_bf16_f32 v0, v9, v10
	v_cvt_pk_bf16_f32 v1, v11, v12
	v_fmac_f32_e32 v21, v3, v29
	v_cvt_pk_bf16_f32 v2, v13, v14
	v_cvt_pk_bf16_f32 v3, v15, v21
	global_store_dwordx4 v[18:19], v[0:3], off offset:256
	v_med3_f32 v4, v14, s49, v254
	s_add_u32 s6, s18, s95
	v_med3_f32 v0, v9, s49, v254
	v_med3_f32 v1, v10, s49, v254
	v_cvt_pk_fp8_f32 v0, v0, v1
	v_med3_f32 v1, v13, s49, v254
	v_cvt_pk_fp8_f32 v1, v1, v4
	v_med3_f32 v2, v11, s49, v254
	v_med3_f32 v3, v12, s49, v254
	v_cvt_pk_fp8_f32 v0, v2, v3 op_sel:[0,0,1]
	v_med3_f32 v2, v15, s49, v254
	v_med3_f32 v3, v21, s49, v254
	v_cvt_pk_fp8_f32 v1, v2, v3 op_sel:[0,0,1]
	v_mul_f32_e32 v2, v10, v10
	v_mul_f32_e32 v3, v12, v12
	v_fmac_f32_e32 v2, v9, v9
	v_fmac_f32_e32 v3, v11, v11
	v_add_f32_e32 v2, v2, v3
	v_mul_f32_e32 v3, v14, v14
	v_mul_f32_e32 v4, v21, v21
	v_fmac_f32_e32 v3, v13, v13
	v_fmac_f32_e32 v4, v15, v15
	v_add_f32_e32 v3, v3, v4
	v_add_f32_e32 v2, v2, v3
	v_add_f32_e32 v4, v8, v2
	ds_swizzle_b32 v5, v4 offset:swizzle(SWAP,16)
	s_addc_u32 s7, s19, s96
	v_lshl_add_u64 v[2:3], s[6:7], 0, v[16:17]
	global_store_dwordx2 v[2:3], v[0:1], off
	s_waitcnt lgkmcnt(0)
	v_add_f32_e32 v0, v4, v5
	v_mov_b32_e32 v1, v0
	s_nop 1
	v_permlane32_swap_b32_e32 v0, v1
	s_and_saveexec_b64 s[6:7], vcc
	s_cbranch_execz .LBB0_1963
	s_lshl_b32 s28, s31, 2
	v_add_f32_e32 v2, v0, v1
	s_ashr_i32 s29, s28, 31
	v_lshl_add_u64 v[0:1], s[12:13], 0, v[56:57]
	v_lshl_add_u64 v[0:1], s[28:29], 2, v[0:1]
	s_lshl_b32 s28, s59, 2
	s_mov_b32 s29, s40
	v_lshl_add_u64 v[0:1], v[0:1], 0, s[28:29]
	global_store_dword v[0:1], v2, off
